# bit-trick f32->bf16 pairs replaced by v_cvt_pk_bf16_f32 (433 sites)
# speedup vs baseline: 1.0014x; 1.0014x over previous
.LBB0_155:
	s_waitcnt lgkmcnt(0)
	ds_read2_b32 v[8:9], v81 offset1:8
	ds_read2_b32 v[12:13], v81 offset0:33 offset1:41
	ds_read2_b32 v[14:15], v81 offset0:66 offset1:74
	ds_read2_b32 v[16:17], v81 offset0:99 offset1:107
	ds_read2_b32 v[18:19], v81 offset0:132 offset1:140
	ds_read2_b32 v[20:21], v81 offset0:165 offset1:173
	s_waitcnt lgkmcnt(5)
	s_waitcnt lgkmcnt(4)
	v_cvt_pk_bf16_f32 v4, v8, v12
	s_waitcnt lgkmcnt(3)
	s_waitcnt lgkmcnt(2)
	ds_read2_b32 v[22:23], v81 offset0:198 offset1:206
	ds_read2_b32 v[24:25], v81 offset0:231 offset1:239
	v_cvt_pk_bf16_f32 v5, v14, v16
	s_waitcnt lgkmcnt(3)
	s_waitcnt lgkmcnt(2)
	v_cvt_pk_bf16_f32 v6, v18, v20
	s_waitcnt lgkmcnt(1)
	s_waitcnt lgkmcnt(0)
	s_lshl_b32 s92, s29, 1
	v_cvt_pk_bf16_f32 v7, v22, v24
	v_or_b32_e32 v2, s28, v79
	v_lshl_add_u64 v[10:11], v[72:73], 0, s[92:93]
	v_lshlrev_b32_e32 v2, 9, v2
	v_lshl_add_u64 v[26:27], v[10:11], 0, v[2:3]
	global_store_dwordx4 v[26:27], v[4:7], off
	s_nop 1
	v_cvt_pk_bf16_f32 v4, v9, v13
	s_nop 0
	v_cvt_pk_bf16_f32 v5, v15, v17
	v_cvt_pk_bf16_f32 v6, v19, v21
	v_cvt_pk_bf16_f32 v7, v23, v25
	v_or_b32_e32 v2, s28, v82
	v_lshlrev_b32_e32 v2, 9, v2
	ds_read2_b32 v[8:9], v81 offset0:16 offset1:24
	v_lshl_add_u64 v[12:13], v[10:11], 0, v[2:3]
	global_store_dwordx4 v[12:13], v[4:7], off
	ds_read2_b32 v[12:13], v81 offset0:49 offset1:57
	ds_read2_b32 v[14:15], v81 offset0:82 offset1:90
	ds_read2_b32 v[16:17], v81 offset0:115 offset1:123
	s_waitcnt lgkmcnt(3)
	s_waitcnt lgkmcnt(2)
	ds_read2_b32 v[18:19], v81 offset0:148 offset1:156
	ds_read2_b32 v[20:21], v81 offset0:181 offset1:189
	v_cvt_pk_bf16_f32 v4, v8, v12
	s_waitcnt lgkmcnt(3)
	s_waitcnt lgkmcnt(2)
	ds_read2_b32 v[22:23], v81 offset0:214 offset1:222
	ds_read2_b32 v[24:25], v81 offset0:247 offset1:255
	v_cvt_pk_bf16_f32 v5, v14, v16
	s_waitcnt lgkmcnt(3)
	s_waitcnt lgkmcnt(2)
	v_cvt_pk_bf16_f32 v6, v18, v20
	s_waitcnt lgkmcnt(1)
	s_waitcnt lgkmcnt(0)
	v_cvt_pk_bf16_f32 v7, v22, v24
	v_or_b32_e32 v2, s28, v83
	v_lshlrev_b32_e32 v2, 9, v2
	v_lshl_add_u64 v[26:27], v[10:11], 0, v[2:3]
	global_store_dwordx4 v[26:27], v[4:7], off
	s_nop 1
	v_cvt_pk_bf16_f32 v4, v9, v13
	s_nop 0
	v_cvt_pk_bf16_f32 v5, v15, v17
	v_cvt_pk_bf16_f32 v6, v19, v21
	v_cvt_pk_bf16_f32 v7, v23, v25
	v_or_b32_e32 v2, s28, v84
	v_lshlrev_b32_e32 v2, 9, v2
	v_lshl_add_u64 v[8:9], v[10:11], 0, v[2:3]
	global_store_dwordx4 v[8:9], v[4:7], off
	s_waitcnt lgkmcnt(0)
	s_mov_b64 s[0:1], 0

.LBB0_165:
	s_and_b32 s0, s2, 0x7c0
	v_or_b32_e32 v80, s0, v74
	v_lshl_add_u64 v[98:99], v[2:3], 1, s[8:9]
	v_lshlrev_b32_e32 v2, 11, v80
	v_lshl_add_u64 v[102:103], v[98:99], 0, v[2:3]
	s_waitcnt vmcnt(15)
	v_bfe_u32 v2, v4, 16, 1
	v_add3_u32 v2, v4, v2, s86
	s_waitcnt vmcnt(14)
	v_bfe_u32 v4, v8, 16, 1
	v_lshrrev_b32_e32 v2, 16, v2
	v_add3_u32 v4, v8, v4, s86
	v_and_or_b32 v98, v4, s87, v2
	s_waitcnt vmcnt(13)
	s_waitcnt vmcnt(12)
	v_cvt_pk_bf16_f32 v99, v12, v16
	s_waitcnt vmcnt(11)
	s_waitcnt vmcnt(10)
	v_cvt_pk_bf16_f32 v100, v20, v24
	s_waitcnt vmcnt(9)
	s_waitcnt vmcnt(8)
	v_cvt_pk_bf16_f32 v101, v28, v32
	s_waitcnt vmcnt(7)
	s_waitcnt vmcnt(6)
	global_store_dwordx4 v[102:103], v[98:101], off
	s_movk_i32 s0, 0x1000
	v_add_co_u32_e32 v8, vcc, s0, v102
	v_cvt_pk_bf16_f32 v98, v36, v40
	s_waitcnt vmcnt(6)
	s_waitcnt vmcnt(5)
	v_cvt_pk_bf16_f32 v99, v44, v48
	s_waitcnt vmcnt(4)
	s_waitcnt vmcnt(3)
	v_cvt_pk_bf16_f32 v100, v52, v56
	s_waitcnt vmcnt(2)
	s_waitcnt vmcnt(1)
	v_cvt_pk_bf16_f32 v101, v64, v60
	v_bfe_u32 v2, v5, 16, 1
	v_add3_u32 v2, v5, v2, s86
	v_bfe_u32 v4, v9, 16, 1
	v_lshrrev_b32_e32 v2, 16, v2
	v_add3_u32 v4, v9, v4, s86
	global_store_dwordx4 v[102:103], v[98:101], off offset:16
	v_addc_co_u32_e32 v9, vcc, 0, v103, vcc
	s_nop 0
	s_nop 1
	v_and_or_b32 v98, v4, s87, v2
	v_cvt_pk_bf16_f32 v99, v13, v17
	v_cvt_pk_bf16_f32 v100, v21, v25
	v_cvt_pk_bf16_f32 v101, v29, v33
	global_store_dwordx4 v[102:103], v[98:101], off offset:2048
	s_nop 1
	v_cvt_pk_bf16_f32 v98, v37, v41
	s_nop 0
	v_cvt_pk_bf16_f32 v99, v45, v49
	v_cvt_pk_bf16_f32 v100, v53, v57
	v_cvt_pk_bf16_f32 v101, v65, v61
	v_bfe_u32 v2, v6, 16, 1
	v_add3_u32 v2, v6, v2, s86
	v_bfe_u32 v4, v10, 16, 1
	v_lshrrev_b32_e32 v2, 16, v2
	v_add3_u32 v4, v10, v4, s86
	global_store_dwordx4 v[102:103], v[98:101], off offset:2064
	s_nop 1
	v_and_or_b32 v98, v4, s87, v2
	s_nop 0
	v_cvt_pk_bf16_f32 v99, v14, v18
	v_cvt_pk_bf16_f32 v100, v22, v26
	v_cvt_pk_bf16_f32 v101, v30, v34
	global_store_dwordx4 v[8:9], v[98:101], off
	s_nop 1
	v_cvt_pk_bf16_f32 v98, v38, v42
	v_cvt_pk_bf16_f32 v99, v46, v50
	v_cvt_pk_bf16_f32 v100, v54, v58
	v_cvt_pk_bf16_f32 v101, v66, v62
	v_cvt_pk_bf16_f32 v4, v7, v11
	v_cvt_pk_bf16_f32 v5, v15, v19
	v_cvt_pk_bf16_f32 v6, v23, v27
	v_cvt_pk_bf16_f32 v7, v31, v35
	global_store_dwordx4 v[8:9], v[4:7], off offset:2048
	s_nop 1
	v_cvt_pk_bf16_f32 v4, v39, v43
	s_nop 0
	v_cvt_pk_bf16_f32 v5, v47, v51
	v_cvt_pk_bf16_f32 v6, v55, v59
	v_cvt_pk_bf16_f32 v7, v67, v63
	global_store_dwordx4 v[8:9], v[98:101], off offset:16
	global_store_dwordx4 v[8:9], v[4:7], off offset:2064

.LBB0_172:
	v_or_b32_e32 v80, s2, v74
	v_lshl_add_u64 v[98:99], v[2:3], 1, s[10:11]
	v_lshlrev_b32_e32 v2, 11, v80
	v_lshl_add_u64 v[102:103], v[98:99], 0, v[2:3]
	s_waitcnt vmcnt(1)
	v_bfe_u32 v2, v64, 16, 1
	v_add3_u32 v2, v64, v2, s86
	v_bfe_u32 v64, v8, 16, 1
	v_lshrrev_b32_e32 v2, 16, v2
	v_add3_u32 v8, v8, v64, s86
	v_and_or_b32 v98, v8, s87, v2
	v_bfe_u32 v2, v4, 16, 1
	v_add3_u32 v2, v4, v2, s86
	v_bfe_u32 v4, v20, 16, 1
	v_lshrrev_b32_e32 v2, 16, v2
	v_add3_u32 v4, v20, v4, s86
	v_and_or_b32 v99, v4, s87, v2
	v_cvt_pk_bf16_f32 v100, v16, v44
	v_cvt_pk_bf16_f32 v101, v32, v52
	global_store_dwordx4 v[102:103], v[98:101], off
	s_movk_i32 s0, 0x1000
	v_add_co_u32_e32 v8, vcc, s0, v102
	v_cvt_pk_bf16_f32 v98, v12, v36
	v_cvt_pk_bf16_f32 v99, v24, v40
	v_cvt_pk_bf16_f32 v100, v28, v56
	s_waitcnt vmcnt(1)
	v_cvt_pk_bf16_f32 v101, v48, v60
	v_bfe_u32 v2, v65, 16, 1
	v_add3_u32 v2, v65, v2, s86
	v_bfe_u32 v4, v9, 16, 1
	v_lshrrev_b32_e32 v2, 16, v2
	v_add3_u32 v4, v9, v4, s86
	global_store_dwordx4 v[102:103], v[98:101], off offset:16
	v_addc_co_u32_e32 v9, vcc, 0, v103, vcc
	s_nop 0
	s_nop 1
	v_and_or_b32 v98, v4, s87, v2
	v_cvt_pk_bf16_f32 v99, v5, v21
	v_cvt_pk_bf16_f32 v100, v17, v45
	v_cvt_pk_bf16_f32 v101, v33, v53
	global_store_dwordx4 v[102:103], v[98:101], off offset:2048
	s_nop 1
	v_cvt_pk_bf16_f32 v98, v13, v37
	s_nop 0
	v_cvt_pk_bf16_f32 v99, v25, v41
	v_cvt_pk_bf16_f32 v100, v29, v57
	v_cvt_pk_bf16_f32 v101, v49, v61
	global_store_dwordx4 v[102:103], v[98:101], off offset:2064
	s_nop 1
	v_cvt_pk_bf16_f32 v98, v66, v10
	v_cvt_pk_bf16_f32 v99, v6, v22
	v_cvt_pk_bf16_f32 v100, v18, v46
	v_cvt_pk_bf16_f32 v101, v34, v54
	global_store_dwordx4 v[8:9], v[98:101], off
	s_nop 1
	v_cvt_pk_bf16_f32 v98, v14, v38
	s_nop 0
	v_cvt_pk_bf16_f32 v99, v26, v42
	v_cvt_pk_bf16_f32 v100, v30, v58
	v_cvt_pk_bf16_f32 v101, v50, v62
	v_cvt_pk_bf16_f32 v4, v67, v11
	v_cvt_pk_bf16_f32 v5, v7, v23
	v_cvt_pk_bf16_f32 v6, v19, v47
	v_cvt_pk_bf16_f32 v7, v35, v55
	global_store_dwordx4 v[8:9], v[4:7], off offset:2048
	s_nop 1
	v_cvt_pk_bf16_f32 v4, v15, v39
	s_nop 0
	v_cvt_pk_bf16_f32 v5, v27, v43
	v_cvt_pk_bf16_f32 v6, v31, v59
	v_cvt_pk_bf16_f32 v7, v51, v63
	global_store_dwordx4 v[8:9], v[98:101], off offset:16
	global_store_dwordx4 v[8:9], v[4:7], off offset:2064

.LBB0_179:
	v_or_b32_e32 v80, s2, v74
	v_lshl_add_u64 v[98:99], v[2:3], 1, s[12:13]
	v_lshlrev_b32_e32 v2, 11, v80
	v_lshl_add_u64 v[102:103], v[98:99], 0, v[2:3]
	s_waitcnt vmcnt(1)
	v_bfe_u32 v2, v64, 16, 1
	v_add3_u32 v2, v64, v2, s86
	v_bfe_u32 v64, v8, 16, 1
	v_lshrrev_b32_e32 v2, 16, v2
	v_add3_u32 v8, v8, v64, s86
	v_and_or_b32 v98, v8, s87, v2
	v_bfe_u32 v2, v4, 16, 1
	v_add3_u32 v2, v4, v2, s86
	v_bfe_u32 v4, v20, 16, 1
	v_lshrrev_b32_e32 v2, 16, v2
	v_add3_u32 v4, v20, v4, s86
	v_and_or_b32 v99, v4, s87, v2
	v_cvt_pk_bf16_f32 v100, v16, v44
	v_cvt_pk_bf16_f32 v101, v32, v52
	global_store_dwordx4 v[102:103], v[98:101], off
	s_movk_i32 s0, 0x1000
	v_add_co_u32_e32 v8, vcc, s0, v102
	v_cvt_pk_bf16_f32 v98, v12, v36
	v_cvt_pk_bf16_f32 v99, v24, v40
	v_cvt_pk_bf16_f32 v100, v28, v56
	s_waitcnt vmcnt(1)
	v_cvt_pk_bf16_f32 v101, v48, v60
	v_bfe_u32 v2, v65, 16, 1
	v_add3_u32 v2, v65, v2, s86
	v_bfe_u32 v4, v9, 16, 1
	v_lshrrev_b32_e32 v2, 16, v2
	v_add3_u32 v4, v9, v4, s86
	global_store_dwordx4 v[102:103], v[98:101], off offset:16
	v_addc_co_u32_e32 v9, vcc, 0, v103, vcc
	s_nop 0
	s_nop 1
	v_and_or_b32 v98, v4, s87, v2
	v_cvt_pk_bf16_f32 v99, v5, v21
	v_cvt_pk_bf16_f32 v100, v17, v45
	v_cvt_pk_bf16_f32 v101, v33, v53
	global_store_dwordx4 v[102:103], v[98:101], off offset:2048
	s_nop 1
	v_cvt_pk_bf16_f32 v98, v13, v37
	s_nop 0
	v_cvt_pk_bf16_f32 v99, v25, v41
	v_cvt_pk_bf16_f32 v100, v29, v57
	v_cvt_pk_bf16_f32 v101, v49, v61
	global_store_dwordx4 v[102:103], v[98:101], off offset:2064
	s_nop 1
	v_cvt_pk_bf16_f32 v98, v66, v10
	v_cvt_pk_bf16_f32 v99, v6, v22
	v_cvt_pk_bf16_f32 v100, v18, v46
	v_cvt_pk_bf16_f32 v101, v34, v54
	global_store_dwordx4 v[8:9], v[98:101], off
	s_nop 1
	v_cvt_pk_bf16_f32 v98, v14, v38
	s_nop 0
	v_cvt_pk_bf16_f32 v99, v26, v42
	v_cvt_pk_bf16_f32 v100, v30, v58
	v_cvt_pk_bf16_f32 v101, v50, v62
	v_cvt_pk_bf16_f32 v4, v67, v11
	v_cvt_pk_bf16_f32 v5, v7, v23
	v_cvt_pk_bf16_f32 v6, v19, v47
	v_cvt_pk_bf16_f32 v7, v35, v55
	global_store_dwordx4 v[8:9], v[4:7], off offset:2048
	s_nop 1
	v_cvt_pk_bf16_f32 v4, v15, v39
	s_nop 0
	v_cvt_pk_bf16_f32 v5, v27, v43
	v_cvt_pk_bf16_f32 v6, v31, v59
	v_cvt_pk_bf16_f32 v7, v51, v63
	global_store_dwordx4 v[8:9], v[98:101], off offset:16
	global_store_dwordx4 v[8:9], v[4:7], off offset:2064

.LBB0_188:
	v_or_b32_e32 v100, s20, v74
	v_lshlrev_b32_e32 v2, 1, v80
	v_lshl_add_u64 v[98:99], s[14:15], 0, v[2:3]
	v_lshlrev_b32_e32 v2, 8, v100
	v_lshl_add_u64 v[102:103], v[98:99], 0, v[2:3]
	s_waitcnt vmcnt(15)
	v_bfe_u32 v2, v8, 16, 1
	v_add3_u32 v2, v8, v2, s86
	s_waitcnt vmcnt(14)
	v_bfe_u32 v8, v4, 16, 1
	v_lshrrev_b32_e32 v2, 16, v2
	v_add3_u32 v4, v4, v8, s86
	v_and_or_b32 v98, v4, s87, v2
	s_waitcnt vmcnt(13)
	s_waitcnt vmcnt(12)
	v_cvt_pk_bf16_f32 v99, v16, v12
	s_waitcnt vmcnt(11)
	s_waitcnt vmcnt(10)
	v_cvt_pk_bf16_f32 v100, v24, v20
	s_waitcnt vmcnt(9)
	s_waitcnt vmcnt(8)
	v_cvt_pk_bf16_f32 v101, v36, v28
	s_waitcnt vmcnt(7)
	s_waitcnt vmcnt(6)
	global_store_dwordx4 v[102:103], v[98:101], off
	s_nop 1
	v_cvt_pk_bf16_f32 v98, v40, v32
	s_waitcnt vmcnt(6)
	s_waitcnt vmcnt(5)
	v_cvt_pk_bf16_f32 v99, v48, v44
	s_waitcnt vmcnt(4)
	s_waitcnt vmcnt(3)
	v_cvt_pk_bf16_f32 v100, v56, v52
	s_waitcnt vmcnt(2)
	s_waitcnt vmcnt(1)
	v_cvt_pk_bf16_f32 v101, v64, v60
	v_bfe_u32 v2, v9, 16, 1
	v_add3_u32 v2, v9, v2, s86
	v_bfe_u32 v4, v5, 16, 1
	v_lshrrev_b32_e32 v2, 16, v2
	v_add3_u32 v4, v5, v4, s86
	global_store_dwordx4 v[102:103], v[98:101], off offset:16
	s_nop 1
	v_and_or_b32 v98, v4, s87, v2
	s_nop 0
	v_cvt_pk_bf16_f32 v99, v17, v13
	v_cvt_pk_bf16_f32 v100, v25, v21
	v_cvt_pk_bf16_f32 v101, v37, v29
	global_store_dwordx4 v[102:103], v[98:101], off offset:256
	s_nop 1
	v_cvt_pk_bf16_f32 v98, v41, v33
	v_cvt_pk_bf16_f32 v99, v49, v45
	v_cvt_pk_bf16_f32 v100, v57, v53
	v_cvt_pk_bf16_f32 v101, v65, v61
	v_bfe_u32 v2, v10, 16, 1
	v_add3_u32 v2, v10, v2, s86
	v_bfe_u32 v4, v6, 16, 1
	v_lshrrev_b32_e32 v2, 16, v2
	v_add3_u32 v4, v6, v4, s86
	global_store_dwordx4 v[102:103], v[98:101], off offset:272
	s_nop 1
	v_and_or_b32 v98, v4, s87, v2
	s_nop 0
	v_cvt_pk_bf16_f32 v99, v18, v14
	v_cvt_pk_bf16_f32 v100, v26, v22
	v_cvt_pk_bf16_f32 v101, v38, v30
	global_store_dwordx4 v[102:103], v[98:101], off offset:512
	s_nop 1
	v_cvt_pk_bf16_f32 v98, v42, v34
	v_cvt_pk_bf16_f32 v99, v50, v46
	v_cvt_pk_bf16_f32 v100, v58, v54
	v_cvt_pk_bf16_f32 v101, v66, v62
	v_cvt_pk_bf16_f32 v4, v11, v7
	v_cvt_pk_bf16_f32 v5, v19, v15
	v_cvt_pk_bf16_f32 v6, v27, v23
	v_cvt_pk_bf16_f32 v7, v39, v31
	global_store_dwordx4 v[102:103], v[4:7], off offset:768
	s_nop 1
	v_cvt_pk_bf16_f32 v4, v43, v35
	s_nop 0
	v_cvt_pk_bf16_f32 v5, v51, v47
	v_cvt_pk_bf16_f32 v6, v59, v55
	v_cvt_pk_bf16_f32 v7, v67, v63
	global_store_dwordx4 v[102:103], v[98:101], off offset:528
	global_store_dwordx4 v[102:103], v[4:7], off offset:784

.LBB0_190:
	s_sub_i32 s0, 0, s5
	s_mul_hi_u32 s1, s0, 0xcccccccd
	s_lshr_b32 s1, s1, 5
	s_mul_i32 s2, s1, 40
	s_sub_i32 s0, s0, s2
	s_lshl_b32 s2, s0, 6
	s_sub_i32 s0, 0, s2
	s_lshl_b32 s1, s1, 6
	v_subrev_u32_e32 v98, s1, v85
	s_ashr_i32 s1, s0, 31
	v_lshl_add_u64 v[28:29], s[0:1], 2, v[76:77]
	v_or_b32_e32 v2, 1, v98
	v_mad_i64_i32 v[4:5], s[0:1], v98, s33, v[28:29]
	v_mad_i64_i32 v[6:7], s[0:1], v2, s33, v[28:29]
	v_or_b32_e32 v2, 2, v98
	global_load_dwordx4 v[48:51], v[4:5], off offset:1664
	global_load_dwordx4 v[12:15], v[6:7], off offset:1664
	v_mad_i64_i32 v[4:5], s[0:1], v2, s33, v[28:29]
	v_or_b32_e32 v2, 3, v98
	v_mad_i64_i32 v[6:7], s[0:1], v2, s33, v[28:29]
	v_or_b32_e32 v2, 4, v98
	global_load_dwordx4 v[60:63], v[4:5], off offset:1664
	global_load_dwordx4 v[32:35], v[6:7], off offset:1664
	v_mad_i64_i32 v[4:5], s[0:1], v2, s33, v[28:29]
	v_or_b32_e32 v2, 5, v98
	global_load_dwordx4 v[36:39], v[4:5], off offset:1664
	v_mad_i64_i32 v[4:5], s[0:1], v2, s33, v[28:29]
	global_load_dwordx4 v[40:43], v[4:5], off offset:1664
	v_or_b32_e32 v2, 6, v98
	v_mad_i64_i32 v[4:5], s[0:1], v2, s33, v[28:29]
	v_or_b32_e32 v2, 7, v98
	v_mad_i64_i32 v[6:7], s[0:1], v2, s33, v[28:29]
	global_load_dwordx4 v[64:67], v[4:5], off offset:1664
	global_load_dwordx4 v[52:55], v[6:7], off offset:1664
	v_or_b32_e32 v2, 8, v98
	v_mad_i64_i32 v[4:5], s[0:1], v2, s33, v[28:29]
	v_or_b32_e32 v2, 9, v98
	v_mad_i64_i32 v[6:7], s[0:1], v2, s33, v[28:29]
	global_load_dwordx4 v[16:19], v[4:5], off offset:1664
	s_nop 0
	global_load_dwordx4 v[4:7], v[6:7], off offset:1664
	v_or_b32_e32 v2, 10, v98
	v_mad_i64_i32 v[8:9], s[0:1], v2, s33, v[28:29]
	v_or_b32_e32 v2, 11, v98
	v_mad_i64_i32 v[10:11], s[0:1], v2, s33, v[28:29]
	global_load_dwordx4 v[44:47], v[8:9], off offset:1664
	s_nop 0
	global_load_dwordx4 v[8:11], v[10:11], off offset:1664
	v_or_b32_e32 v2, 12, v98
	v_mad_i64_i32 v[20:21], s[0:1], v2, s33, v[28:29]
	v_or_b32_e32 v2, 13, v98
	v_mad_i64_i32 v[22:23], s[0:1], v2, s33, v[28:29]
	global_load_dwordx4 v[56:59], v[20:21], off offset:1664
	s_nop 0
	global_load_dwordx4 v[20:23], v[22:23], off offset:1664
	v_or_b32_e32 v2, 14, v98
	v_mad_i64_i32 v[24:25], s[0:1], v2, s33, v[28:29]
	v_or_b32_e32 v2, 15, v98
	global_load_dwordx4 v[24:27], v[24:25], off offset:1664
	v_mad_i64_i32 v[28:29], s[0:1], v2, s33, v[28:29]
	global_load_dwordx4 v[28:31], v[28:29], off offset:1664
	v_subrev_u32_e32 v102, s2, v74
	v_ashrrev_i32_e32 v99, 31, v98
	v_ashrrev_i32_e32 v103, 31, v102
	v_lshl_add_u64 v[104:105], v[98:99], 1, s[16:17]
	v_lshlrev_b64 v[98:99], 11, v[102:103]
	v_lshl_add_u64 v[106:107], v[104:105], 0, v[98:99]
	s_waitcnt vmcnt(15)
	v_bfe_u32 v2, v48, 16, 1
	s_waitcnt vmcnt(14)
	v_bfe_u32 v80, v12, 16, 1
	v_add3_u32 v2, v48, v2, s86
	v_add3_u32 v12, v12, v80, s86
	v_lshrrev_b32_e32 v2, 16, v2
	s_waitcnt vmcnt(13)
	v_bfe_u32 v98, v60, 16, 1
	v_add3_u32 v48, v60, v98, s86
	v_and_or_b32 v98, v12, s87, v2
	s_waitcnt vmcnt(12)
	v_bfe_u32 v99, v32, 16, 1
	v_add3_u32 v32, v32, v99, s86
	s_waitcnt vmcnt(11)
	v_bfe_u32 v100, v36, 16, 1
	v_add3_u32 v36, v36, v100, s86
	v_lshrrev_b32_e32 v2, 16, v36
	s_waitcnt vmcnt(10)
	v_bfe_u32 v12, v40, 16, 1
	v_add3_u32 v12, v40, v12, s86
	v_and_or_b32 v100, v12, s87, v2
	v_lshrrev_b32_e32 v48, 16, v48
	v_and_or_b32 v99, v32, s87, v48
	s_waitcnt vmcnt(9)
	s_waitcnt vmcnt(8)
	v_cvt_pk_bf16_f32 v101, v64, v52
	global_store_dwordx4 v[106:107], v[98:101], off
	s_waitcnt vmcnt(8)
	v_bfe_u32 v2, v16, 16, 1
	v_add3_u32 v2, v16, v2, s86
	s_waitcnt vmcnt(7)
	v_bfe_u32 v12, v4, 16, 1
	v_lshrrev_b32_e32 v2, 16, v2
	v_add3_u32 v4, v4, v12, s86
	v_and_or_b32 v98, v4, s87, v2
	s_waitcnt vmcnt(6)
	s_waitcnt vmcnt(5)
	v_cvt_pk_bf16_f32 v99, v44, v8
	s_waitcnt vmcnt(4)
	s_waitcnt vmcnt(3)
	v_cvt_pk_bf16_f32 v100, v56, v20
	s_waitcnt vmcnt(2)
	s_waitcnt vmcnt(1)
	v_cvt_pk_bf16_f32 v101, v24, v28
	global_store_dwordx4 v[106:107], v[98:101], off offset:16
	s_nop 1
	v_or_b32_e32 v98, 1, v102
	s_nop 0
	v_ashrrev_i32_e32 v99, 31, v98
	v_lshlrev_b64 v[98:99], 11, v[98:99]
	v_lshl_add_u64 v[106:107], v[104:105], 0, v[98:99]
	v_cvt_pk_bf16_f32 v98, v49, v13
	v_cvt_pk_bf16_f32 v99, v61, v33
	v_cvt_pk_bf16_f32 v100, v37, v41
	v_cvt_pk_bf16_f32 v101, v65, v53
	global_store_dwordx4 v[106:107], v[98:101], off
	s_nop 0
	s_nop 0
	v_cvt_pk_bf16_f32 v98, v17, v5
	v_cvt_pk_bf16_f32 v99, v45, v9
	v_cvt_pk_bf16_f32 v100, v57, v21
	v_cvt_pk_bf16_f32 v101, v25, v29
	global_store_dwordx4 v[106:107], v[98:101], off offset:16
	v_or_b32_e32 v4, 2, v102
	v_ashrrev_i32_e32 v5, 31, v4
	v_cvt_pk_bf16_f32 v98, v50, v14
	v_cvt_pk_bf16_f32 v99, v62, v34
	v_cvt_pk_bf16_f32 v100, v38, v42
	v_cvt_pk_bf16_f32 v101, v66, v54
	v_bfe_u32 v2, v18, 16, 1
	v_lshlrev_b64 v[4:5], 11, v[4:5]
	v_add3_u32 v2, v18, v2, s86
	v_bfe_u32 v8, v6, 16, 1
	v_lshl_add_u64 v[4:5], v[104:105], 0, v[4:5]
	v_lshrrev_b32_e32 v2, 16, v2
	v_add3_u32 v6, v6, v8, s86
	global_store_dwordx4 v[4:5], v[98:101], off
	s_nop 1
	v_and_or_b32 v98, v6, s87, v2
	v_cvt_pk_bf16_f32 v99, v46, v10
	v_cvt_pk_bf16_f32 v100, v58, v22
	v_cvt_pk_bf16_f32 v101, v26, v30
	global_store_dwordx4 v[4:5], v[98:101], off offset:16
	v_or_b32_e32 v4, 3, v102
	v_ashrrev_i32_e32 v5, 31, v4
	v_lshlrev_b64 v[4:5], 11, v[4:5]
	v_lshl_add_u64 v[8:9], v[104:105], 0, v[4:5]
	v_cvt_pk_bf16_f32 v12, v51, v15
	v_cvt_pk_bf16_f32 v13, v63, v35
	v_cvt_pk_bf16_f32 v14, v39, v43
	v_cvt_pk_bf16_f32 v15, v67, v55
	v_cvt_pk_bf16_f32 v4, v19, v7
	v_cvt_pk_bf16_f32 v5, v47, v11
	v_cvt_pk_bf16_f32 v6, v59, v23
	v_bfe_u32 v2, v27, 16, 1
	v_add3_u32 v2, v27, v2, s86
	v_bfe_u32 v7, v31, 16, 1
	v_lshrrev_b32_e32 v2, 16, v2
	v_add3_u32 v7, v31, v7, s86
	v_and_or_b32 v7, v7, s87, v2
	global_store_dwordx4 v[8:9], v[12:15], off
	global_store_dwordx4 v[8:9], v[4:7], off offset:16
	s_branch .LBB0_121

.LBB0_193:
	v_or_b32_e32 v80, s2, v74
	v_lshl_add_u64 v[98:99], v[2:3], 1, s[6:7]
	v_lshlrev_b32_e32 v2, 11, v80
	v_lshl_add_u64 v[102:103], v[98:99], 0, v[2:3]
	s_waitcnt vmcnt(1)
	v_bfe_u32 v2, v64, 16, 1
	v_add3_u32 v2, v64, v2, s86
	v_bfe_u32 v64, v8, 16, 1
	v_lshrrev_b32_e32 v2, 16, v2
	v_add3_u32 v8, v8, v64, s86
	v_and_or_b32 v98, v8, s87, v2
	v_bfe_u32 v2, v4, 16, 1
	v_add3_u32 v2, v4, v2, s86
	v_bfe_u32 v4, v20, 16, 1
	v_lshrrev_b32_e32 v2, 16, v2
	v_add3_u32 v4, v20, v4, s86
	v_and_or_b32 v99, v4, s87, v2
	v_cvt_pk_bf16_f32 v100, v16, v44
	v_cvt_pk_bf16_f32 v101, v32, v52
	global_store_dwordx4 v[102:103], v[98:101], off
	s_movk_i32 s0, 0x1000
	v_add_co_u32_e32 v8, vcc, s0, v102
	v_cvt_pk_bf16_f32 v98, v12, v36
	v_cvt_pk_bf16_f32 v99, v24, v40
	v_cvt_pk_bf16_f32 v100, v28, v56
	s_waitcnt vmcnt(1)
	v_cvt_pk_bf16_f32 v101, v48, v60
	v_bfe_u32 v2, v65, 16, 1
	v_add3_u32 v2, v65, v2, s86
	v_bfe_u32 v4, v9, 16, 1
	v_lshrrev_b32_e32 v2, 16, v2
	v_add3_u32 v4, v9, v4, s86
	global_store_dwordx4 v[102:103], v[98:101], off offset:16
	v_addc_co_u32_e32 v9, vcc, 0, v103, vcc
	s_nop 0
	s_nop 1
	v_and_or_b32 v98, v4, s87, v2
	v_cvt_pk_bf16_f32 v99, v5, v21
	v_cvt_pk_bf16_f32 v100, v17, v45
	v_cvt_pk_bf16_f32 v101, v33, v53
	global_store_dwordx4 v[102:103], v[98:101], off offset:2048
	s_nop 1
	v_cvt_pk_bf16_f32 v98, v13, v37
	s_nop 0
	v_cvt_pk_bf16_f32 v99, v25, v41
	v_cvt_pk_bf16_f32 v100, v29, v57
	v_cvt_pk_bf16_f32 v101, v49, v61
	global_store_dwordx4 v[102:103], v[98:101], off offset:2064
	s_nop 1
	v_cvt_pk_bf16_f32 v98, v66, v10
	v_cvt_pk_bf16_f32 v99, v6, v22
	v_cvt_pk_bf16_f32 v100, v18, v46
	v_cvt_pk_bf16_f32 v101, v34, v54
	global_store_dwordx4 v[8:9], v[98:101], off
	s_nop 1
	v_cvt_pk_bf16_f32 v98, v14, v38
	s_nop 0
	v_cvt_pk_bf16_f32 v99, v26, v42
	v_cvt_pk_bf16_f32 v100, v30, v58
	v_cvt_pk_bf16_f32 v101, v50, v62
	v_cvt_pk_bf16_f32 v4, v67, v11
	v_cvt_pk_bf16_f32 v5, v7, v23
	v_cvt_pk_bf16_f32 v6, v19, v47
	v_cvt_pk_bf16_f32 v7, v35, v55
	global_store_dwordx4 v[8:9], v[4:7], off offset:2048
	s_nop 1
	v_cvt_pk_bf16_f32 v4, v15, v39
	s_nop 0
	v_cvt_pk_bf16_f32 v5, v27, v43
	v_cvt_pk_bf16_f32 v6, v31, v59
	v_cvt_pk_bf16_f32 v7, v51, v63
	global_store_dwordx4 v[8:9], v[98:101], off offset:16
	global_store_dwordx4 v[8:9], v[4:7], off offset:2064
	s_cbranch_execz .LBB0_161
	s_branch .LBB0_166

.LBB0_732:
	s_cmp_eq_u32 s70, 1
	s_mov_b64 s[26:27], -1
	s_cbranch_scc0 .LBB0_734
	s_waitcnt vmcnt(7)
	s_waitcnt vmcnt(6)
	v_cvt_pk_bf16_f32 v4, v102, v106
	s_waitcnt vmcnt(5)
	s_waitcnt vmcnt(4)
	v_cvt_pk_bf16_f32 v5, v110, v114
	s_waitcnt vmcnt(3)
	s_waitcnt vmcnt(2)
	v_cvt_pk_bf16_f32 v6, v118, v122
	s_waitcnt vmcnt(1)
	s_waitcnt vmcnt(0)
	v_cvt_pk_bf16_f32 v7, v126, v130
	global_store_dwordx4 v[182:183], v[4:7], off
	s_nop 1
	v_cvt_pk_bf16_f32 v4, v103, v107
	s_nop 0
	v_cvt_pk_bf16_f32 v5, v111, v115
	v_cvt_pk_bf16_f32 v6, v119, v123
	v_cvt_pk_bf16_f32 v7, v127, v131
	global_store_dwordx4 v[182:183], v[4:7], off offset:1024
	s_nop 1
	v_cvt_pk_bf16_f32 v4, v104, v108
	s_nop 0
	v_cvt_pk_bf16_f32 v5, v112, v116
	v_cvt_pk_bf16_f32 v6, v120, v124
	v_cvt_pk_bf16_f32 v7, v128, v132
	global_store_dwordx4 v[182:183], v[4:7], off offset:2048
	s_nop 1
	v_cvt_pk_bf16_f32 v4, v105, v109
	s_nop 0
	v_cvt_pk_bf16_f32 v5, v113, v117
	v_cvt_pk_bf16_f32 v6, v121, v125
	v_cvt_pk_bf16_f32 v7, v129, v133
	global_store_dwordx4 v[182:183], v[4:7], off offset:3072
	s_mov_b64 s[26:27], 0

.LBB0_800:
	s_andn2_b64 vcc, exec, s[0:1]
	s_cbranch_vccnz .LBB0_802
	s_waitcnt vmcnt(7)
	s_waitcnt vmcnt(6)
	v_cvt_pk_bf16_f32 v36, v8, v4
	s_waitcnt vmcnt(5)
	s_waitcnt vmcnt(4) lgkmcnt(3)
	v_cvt_pk_bf16_f32 v37, v16, v12
	s_waitcnt vmcnt(3)
	s_waitcnt vmcnt(2)
	v_cvt_pk_bf16_f32 v38, v24, v20
	s_waitcnt vmcnt(1)
	s_waitcnt vmcnt(0)
	v_cvt_pk_bf16_f32 v39, v32, v28
	global_store_dwordx4 v[182:183], v[36:39], off
	s_nop 1
	v_cvt_pk_bf16_f32 v36, v9, v5
	s_nop 0
	v_cvt_pk_bf16_f32 v37, v17, v13
	v_cvt_pk_bf16_f32 v38, v25, v21
	v_cvt_pk_bf16_f32 v39, v33, v29
	global_store_dwordx4 v[182:183], v[36:39], off offset:1024
	s_nop 1
	v_cvt_pk_bf16_f32 v36, v10, v6
	s_nop 0
	v_cvt_pk_bf16_f32 v37, v18, v14
	v_cvt_pk_bf16_f32 v38, v26, v22
	v_cvt_pk_bf16_f32 v39, v34, v30
	global_store_dwordx4 v[182:183], v[36:39], off offset:2048
	s_nop 1
	v_cvt_pk_bf16_f32 v36, v11, v7
	s_nop 0
	v_cvt_pk_bf16_f32 v37, v19, v15
	v_cvt_pk_bf16_f32 v38, v27, v23
	v_cvt_pk_bf16_f32 v39, v35, v31
	global_store_dwordx4 v[182:183], v[36:39], off offset:3072

.LBB0_1202:
	v_lshl_add_u64 v[78:79], s[18:19], 0, v[60:61]
	s_mov_b32 s10, 0x2f200000
	v_add_co_u32_e32 v4, vcc, s10, v78
	s_mov_b32 s11, 0x2e00000
	s_nop 0
	v_addc_co_u32_e32 v5, vcc, 0, v79, vcc
	global_load_dwordx4 v[8:11], v[4:5], off offset:1024
	global_load_dwordx4 v[12:15], v[4:5], off
	s_nop 0
	global_load_dwordx4 v[4:7], v[42:43], off offset:2048
	v_add_co_u32_e32 v78, vcc, s11, v78
	s_add_u32 s40, s36, s8
	s_nop 0
	v_addc_co_u32_e32 v79, vcc, 0, v79, vcc
	s_add_u32 s10, s0, s8
	s_addc_u32 s11, s1, s9
	s_add_i32 s41, s40, 0xffffc000
	s_cmpk_lt_i32 s40, 0x4000
	s_cselect_b32 s10, s10, s41
	s_mov_b32 s41, 0x3e200000
	s_cselect_b32 s41, s41, 0x45200000
	s_cselect_b32 s11, s11, 0
	s_add_u32 s41, s18, s41
	s_addc_u32 s42, s19, 0
	s_lshl_b64 s[10:11], s[10:11], 10
	s_add_u32 s10, s41, s10
	s_addc_u32 s11, s42, s11
	s_waitcnt vmcnt(0)
	v_lshlrev_b32_e32 v62, 16, v8
	v_lshlrev_b32_e32 v70, 16, v12
	v_and_b32_e32 v72, 0xffff0000, v12
	v_add_f32_e32 v2, 0, v70
	v_lshlrev_b32_e32 v71, 16, v13
	v_add_f32_e32 v2, v2, v72
	v_and_b32_e32 v73, 0xffff0000, v13
	v_add_f32_e32 v2, v2, v71
	v_lshlrev_b32_e32 v74, 16, v14
	v_add_f32_e32 v2, v2, v73
	v_and_b32_e32 v76, 0xffff0000, v14
	v_add_f32_e32 v2, v2, v74
	v_lshlrev_b32_e32 v75, 16, v15
	v_add_f32_e32 v2, v2, v76
	v_and_b32_e32 v77, 0xffff0000, v15
	v_add_f32_e32 v2, v2, v75
	v_add_f32_e32 v2, v2, v77
	v_and_b32_e32 v64, 0xffff0000, v8
	v_add_f32_e32 v2, v2, v62
	v_lshlrev_b32_e32 v63, 16, v9
	v_add_f32_e32 v2, v2, v64
	v_and_b32_e32 v65, 0xffff0000, v9
	v_add_f32_e32 v2, v2, v63
	v_lshlrev_b32_e32 v66, 16, v10
	v_add_f32_e32 v2, v2, v65
	v_and_b32_e32 v68, 0xffff0000, v10
	v_add_f32_e32 v2, v2, v66
	v_lshlrev_b32_e32 v67, 16, v11
	v_add_f32_e32 v2, v2, v68
	v_and_b32_e32 v69, 0xffff0000, v11
	v_add_f32_e32 v2, v2, v67
	v_add_f32_e32 v2, v2, v69
	ds_bpermute_b32 v12, v80, v2
	global_load_dwordx4 v[8:11], v[44:45], off offset:2048
	s_waitcnt lgkmcnt(0)
	v_add_f32_e32 v2, v2, v12
	global_load_dwordx4 v[12:15], v[42:43], off offset:2064
	global_load_dwordx4 v[16:19], v[44:45], off offset:2064
	ds_bpermute_b32 v20, v81, v2
	s_waitcnt lgkmcnt(0)
	v_add_f32_e32 v2, v2, v20
	global_load_dwordx4 v[20:23], v[42:43], off offset:16
	global_load_dwordx4 v[24:27], v[42:43], off
	global_load_dwordx4 v[28:31], v[44:45], off offset:16
	global_load_dwordx4 v[32:35], v[44:45], off
	ds_bpermute_b32 v53, v82, v2
	s_waitcnt lgkmcnt(0)
	v_add_f32_e32 v2, v2, v53
	ds_bpermute_b32 v53, v83, v2
	s_waitcnt lgkmcnt(0)
	v_add_f32_e32 v2, v2, v53
	ds_bpermute_b32 v53, v84, v2
	s_waitcnt lgkmcnt(0)
	v_add_f32_e32 v2, v2, v53
	ds_bpermute_b32 v53, v85, v2
	s_waitcnt lgkmcnt(0)
	v_add_f32_e32 v2, v2, v53
	v_mul_f32_e32 v2, 0x3a800000, v2
	v_pk_add_f32 v[70:71], v[70:71], v[2:3] op_sel_hi:[1,0] neg_lo:[0,1] neg_hi:[0,1]
	v_pk_add_f32 v[72:73], v[72:73], v[2:3] op_sel_hi:[1,0] neg_lo:[0,1] neg_hi:[0,1]
	v_pk_mul_f32 v[108:109], v[70:71], v[70:71]
	v_pk_mul_f32 v[110:111], v[72:73], v[72:73]
	v_pk_add_f32 v[74:75], v[74:75], v[2:3] op_sel_hi:[1,0] neg_lo:[0,1] neg_hi:[0,1]
	v_pk_add_f32 v[76:77], v[76:77], v[2:3] op_sel_hi:[1,0] neg_lo:[0,1] neg_hi:[0,1]
	v_pk_add_f32 v[62:63], v[62:63], v[2:3] op_sel_hi:[1,0] neg_lo:[0,1] neg_hi:[0,1]
	v_pk_add_f32 v[64:65], v[64:65], v[2:3] op_sel_hi:[1,0] neg_lo:[0,1] neg_hi:[0,1]
	v_pk_add_f32 v[66:67], v[66:67], v[2:3] op_sel_hi:[1,0] neg_lo:[0,1] neg_hi:[0,1]
	v_pk_add_f32 v[68:69], v[68:69], v[2:3] op_sel_hi:[1,0] neg_lo:[0,1] neg_hi:[0,1]
	v_add_f32_e32 v2, v108, v110
	v_add_f32_e32 v2, v109, v2
	v_pk_mul_f32 v[112:113], v[74:75], v[74:75]
	v_add_f32_e32 v2, v111, v2
	v_pk_mul_f32 v[114:115], v[76:77], v[76:77]
	v_add_f32_e32 v2, v112, v2
	v_add_f32_e32 v2, v114, v2
	v_add_f32_e32 v2, v113, v2
	v_pk_mul_f32 v[116:117], v[62:63], v[62:63]
	v_add_f32_e32 v2, v115, v2
	v_pk_mul_f32 v[118:119], v[64:65], v[64:65]
	v_add_f32_e32 v2, v116, v2
	v_add_f32_e32 v2, v118, v2
	v_mov_b32_e32 v120, v68
	v_mov_b32_e32 v121, v66
	v_add_f32_e32 v2, v117, v2
	v_pk_mul_f32 v[120:121], v[120:121], v[120:121]
	v_add_f32_e32 v2, v119, v2
	v_mov_b32_e32 v122, v69
	v_mov_b32_e32 v123, v67
	v_add_f32_e32 v2, v121, v2
	v_pk_mul_f32 v[122:123], v[122:123], v[122:123]
	v_add_f32_e32 v2, v120, v2
	v_add_f32_e32 v2, v123, v2
	v_add_f32_e32 v2, v122, v2
	ds_bpermute_b32 v53, v80, v2
	v_mov_b32_e32 v108, v4
	v_mov_b32_e32 v109, v6
	v_mov_b32_e32 v6, v5
	s_waitcnt lgkmcnt(0)
	v_add_f32_e32 v2, v2, v53
	ds_bpermute_b32 v4, v81, v2
	s_waitcnt vmcnt(6)
	v_mov_b32_e32 v110, v8
	v_mov_b32_e32 v111, v10
	v_mov_b32_e32 v10, v9
	s_waitcnt lgkmcnt(0)
	v_add_f32_e32 v2, v2, v4
	ds_bpermute_b32 v53, v82, v2
	s_waitcnt vmcnt(4)
	v_mov_b32_e32 v8, v16
	v_mov_b32_e32 v4, v12
	v_mov_b32_e32 v5, v14
	v_mov_b32_e32 v9, v18
	s_waitcnt lgkmcnt(0)
	v_add_f32_e32 v2, v2, v53
	ds_bpermute_b32 v16, v83, v2
	s_waitcnt vmcnt(2)
	v_mov_b32_e32 v12, v24
	v_mov_b32_e32 v14, v13
	v_mov_b32_e32 v18, v17
	v_mov_b32_e32 v13, v26
	s_waitcnt lgkmcnt(0)
	v_add_f32_e32 v2, v2, v16
	ds_bpermute_b32 v24, v84, v2
	s_waitcnt vmcnt(0)
	v_mov_b32_e32 v16, v32
	v_mov_b32_e32 v17, v34
	v_mov_b32_e32 v26, v25
	v_mov_b32_e32 v34, v33
	s_waitcnt lgkmcnt(0)
	v_add_f32_e32 v2, v2, v24
	ds_bpermute_b32 v53, v85, v2
	v_mov_b32_e32 v24, v20
	v_mov_b32_e32 v25, v22
	v_mov_b32_e32 v32, v28
	v_mov_b32_e32 v33, v30
	s_waitcnt lgkmcnt(0)
	v_add_f32_e32 v2, v2, v53
	v_fmamk_f32 v2, v2, 0x3a800000, v237
	v_mul_f32_e32 v20, 0x4b800000, v2
	v_cmp_gt_f32_e32 vcc, s85, v2
	v_mov_b32_e32 v22, v21
	v_mov_b32_e32 v30, v29
	v_cndmask_b32_e32 v2, v2, v20, vcc
	v_rsq_f32_e32 v2, v2
	s_nop 0
	v_mul_f32_e32 v20, 0x45800000, v2
	v_cndmask_b32_e32 v2, v2, v20, vcc
	v_pk_mul_f32 v[20:21], v[70:71], v[2:3] op_sel_hi:[1,0]
	v_pk_mul_f32 v[28:29], v[74:75], v[2:3] op_sel_hi:[1,0]
	v_pk_mul_f32 v[70:71], v[72:73], v[2:3] op_sel_hi:[1,0]
	v_pk_mul_f32 v[64:65], v[64:65], v[2:3] op_sel_hi:[1,0]
	v_pk_fma_f32 v[12:13], v[12:13], v[20:21], v[16:17]
	v_pk_fma_f32 v[16:17], v[24:25], v[28:29], v[32:33]
	v_pk_fma_f32 v[20:21], v[26:27], v[70:71], v[34:35]
	v_pk_mul_f32 v[72:73], v[76:77], v[2:3] op_sel_hi:[1,0]
	v_pk_fma_f32 v[28:29], v[6:7], v[64:65], v[10:11]
	v_bfe_u32 v6, v20, 16, 1
	v_bfe_u32 v10, v17, 16, 1
	v_max3_f32 v35, |v12|, 0, |v20|
	v_pk_fma_f32 v[22:23], v[22:23], v[72:73], v[30:31]
	v_add3_u32 v53, v20, v6, s86
	v_add3_u32 v6, v17, v10, s86
	v_max3_f32 v10, v35, |v13|, |v21|
	v_pk_mul_f32 v[62:63], v[62:63], v[2:3] op_sel_hi:[1,0]
	v_max3_f32 v10, v10, |v16|, |v22|
	v_pk_fma_f32 v[24:25], v[108:109], v[62:63], v[110:111]
	v_max3_f32 v10, v10, |v17|, |v23|
	v_pk_mul_f32 v[66:67], v[66:67], v[2:3] op_sel_hi:[1,0]
	v_pk_mul_f32 v[68:69], v[68:69], v[2:3] op_sel_hi:[1,0]
	v_max3_f32 v10, v10, |v24|, |v28|
	v_pk_fma_f32 v[26:27], v[4:5], v[66:67], v[8:9]
	v_pk_fma_f32 v[14:15], v[14:15], v[68:69], v[18:19]
	v_max3_f32 v10, v10, |v25|, |v29|
	v_max3_f32 v10, v10, |v26|, |v14|
	v_max3_f32 v10, v10, |v27|, |v15|
	ds_bpermute_b32 v35, v80, v10
	v_bfe_u32 v7, v12, 16, 1
	v_add3_u32 v7, v12, v7, s86
	v_lshrrev_b32_e32 v62, 16, v7
	v_bfe_u32 v2, v23, 16, 1
	s_waitcnt lgkmcnt(0)
	v_max_f32_e32 v35, v35, v35
	v_max_f32_e32 v10, v10, v35
	ds_bpermute_b32 v35, v81, v10
	v_add3_u32 v2, v23, v2, s86
	v_lshrrev_b32_e32 v6, 16, v6
	s_waitcnt lgkmcnt(0)
	v_max_f32_e32 v7, v35, v35
	v_max_f32_e32 v7, v10, v7
	ds_bpermute_b32 v10, v82, v7
	s_waitcnt lgkmcnt(0)
	v_max_f32_e32 v10, v10, v10
	v_max_f32_e32 v10, v7, v10
	ds_bpermute_b32 v35, v83, v10
	v_and_or_b32 v7, v2, s87, v6
	v_cvt_pk_bf16_f32 v5, v13, v21
	s_waitcnt lgkmcnt(0)
	v_max_f32_e32 v2, v35, v35
	v_max_f32_e32 v2, v10, v2
	ds_bpermute_b32 v10, v84, v2
	v_cvt_pk_bf16_f32 v11, v27, v15
	s_waitcnt lgkmcnt(0)
	v_max_f32_e32 v8, v10, v10
	v_max_f32_e32 v2, v2, v8
	ds_bpermute_b32 v34, v85, v2
	v_cvt_pk_bf16_f32 v6, v16, v22
	v_and_or_b32 v4, v53, s87, v62
	s_waitcnt lgkmcnt(0)
	v_max3_f32 v2, v2, v34, s55
	global_store_dwordx4 v[78:79], v[4:7], off
	s_nop 1
	v_div_scale_f32 v4, s[42:43], v2, v2, s80
	s_nop 0
	v_rcp_f32_e32 v5, v4
	s_nop 0
	v_fma_f32 v7, -v4, v5, 1.0
	v_div_scale_f32 v6, vcc, s80, v2, s80
	v_fmac_f32_e32 v5, v7, v5
	v_cvt_pk_bf16_f32 v10, v26, v14
	v_cvt_pk_bf16_f32 v9, v25, v29
	v_cvt_pk_bf16_f32 v8, v24, v28
	v_mul_f32_e32 v7, v6, v5
	global_store_dwordx4 v[78:79], v[8:11], off offset:1024
	s_nop 1
	v_fma_f32 v8, -v4, v7, v6
	v_fmac_f32_e32 v7, v8, v5
	v_fma_f32 v4, -v4, v7, v6
	v_div_fmas_f32 v4, v4, v5, v7
	v_div_fixup_f32 v4, v4, v2, s80
	v_mul_f32_e32 v5, v12, v4
	v_mul_f32_e32 v6, v20, v4
	v_rndne_f32_e32 v5, v5
	v_mul_f32_e32 v7, v13, v4
	v_mul_f32_e32 v8, v21, v4
	v_mul_f32_e32 v9, v16, v4
	v_mul_f32_e32 v10, v22, v4
	v_mul_f32_e32 v11, v17, v4
	v_mul_f32_e32 v12, v23, v4
	v_mul_f32_e32 v13, v24, v4
	v_mul_f32_e32 v16, v28, v4
	v_mul_f32_e32 v17, v25, v4
	v_mul_f32_e32 v18, v29, v4
	v_mul_f32_e32 v19, v26, v4
	v_mul_f32_e32 v14, v14, v4
	v_mul_f32_e32 v20, v27, v4
	v_mul_f32_e32 v4, v15, v4
	v_rndne_f32_e32 v6, v6
	v_rndne_f32_e32 v15, v4
	v_add_f32_e32 v4, 0x43000000, v5
	v_rndne_f32_e32 v7, v7
	v_cvt_pk_u8_f32 v4, v4, 0, 0
	v_add_f32_e32 v5, 0x43000000, v6
	v_rndne_f32_e32 v8, v8
	v_cvt_pk_u8_f32 v4, v5, 1, v4
	v_add_f32_e32 v5, 0x43000000, v7
	v_rndne_f32_e32 v9, v9
	v_cvt_pk_u8_f32 v4, v5, 2, v4
	v_add_f32_e32 v5, 0x43000000, v8
	v_rndne_f32_e32 v10, v10
	v_cvt_pk_u8_f32 v4, v5, 3, v4
	v_add_f32_e32 v5, 0x43000000, v9
	v_rndne_f32_e32 v11, v11
	v_cvt_pk_u8_f32 v5, v5, 0, 0
	v_add_f32_e32 v6, 0x43000000, v10
	v_rndne_f32_e32 v12, v12
	v_cvt_pk_u8_f32 v5, v6, 1, v5
	v_add_f32_e32 v6, 0x43000000, v11
	v_rndne_f32_e32 v13, v13
	v_cvt_pk_u8_f32 v5, v6, 2, v5
	v_add_f32_e32 v6, 0x43000000, v12
	v_rndne_f32_e32 v16, v16
	v_cvt_pk_u8_f32 v5, v6, 3, v5
	v_add_f32_e32 v6, 0x43000000, v13
	v_rndne_f32_e32 v17, v17
	v_cvt_pk_u8_f32 v6, v6, 0, 0
	v_add_f32_e32 v7, 0x43000000, v16
	v_rndne_f32_e32 v18, v18
	v_cvt_pk_u8_f32 v6, v7, 1, v6
	v_add_f32_e32 v7, 0x43000000, v17
	v_rndne_f32_e32 v19, v19
	v_cvt_pk_u8_f32 v6, v7, 2, v6
	v_add_f32_e32 v7, 0x43000000, v18
	v_rndne_f32_e32 v14, v14
	v_cvt_pk_u8_f32 v6, v7, 3, v6
	v_add_f32_e32 v7, 0x43000000, v19
	v_rndne_f32_e32 v20, v20
	v_cvt_pk_u8_f32 v7, v7, 0, 0
	v_add_f32_e32 v8, 0x43000000, v14
	v_cvt_pk_u8_f32 v7, v8, 1, v7
	v_add_f32_e32 v8, 0x43000000, v20
	v_cvt_pk_u8_f32 v7, v8, 2, v7
	v_add_f32_e32 v8, 0x43000000, v15
	v_xor_b32_e32 v4, 0x80808080, v4
	v_xor_b32_e32 v5, 0x80808080, v5
	v_cvt_pk_u8_f32 v7, v8, 3, v7
	v_lshl_add_u64 v[8:9], s[10:11], 0, v[38:39]
	v_xor_b32_e32 v6, 0x80808080, v6
	v_xor_b32_e32 v7, 0x80808080, v7
	global_store_dwordx2 v[8:9], v[4:5], off
	global_store_dwordx2 v[8:9], v[6:7], off offset:512
	s_and_saveexec_b64 s[10:11], s[4:5]
	s_cbranch_execz .LBB0_1204
	s_add_u32 s42, s18, s38
	s_addc_u32 s43, s19, s39
	v_mul_f32_e32 v2, 0x3c010204, v2
	global_store_dword v3, v2, s[42:43]
.LBB0_1204:
	s_or_b64 exec, exec, s[10:11]
	v_lshl_add_u64 v[78:79], s[18:19], 0, v[58:59]
	v_add_co_u32_e32 v4, vcc, 0x2f200000, v78
	s_mov_b32 s41, 0x2e00000
	s_nop 0
	v_addc_co_u32_e32 v5, vcc, 0, v79, vcc
	global_load_dwordx4 v[8:11], v[4:5], off offset:1024
	global_load_dwordx4 v[12:15], v[4:5], off
	s_nop 0
	global_load_dwordx4 v[4:7], v[42:43], off offset:2048
	v_add_co_u32_e32 v78, vcc, s41, v78
	s_add_i32 s10, s40, 1
	s_nop 0
	v_addc_co_u32_e32 v79, vcc, 0, v79, vcc
	s_add_u32 s11, s34, s8
	s_addc_u32 s41, s35, s9
	s_add_i32 s42, s40, 0xffffc001
	s_cmpk_lt_i32 s10, 0x4000
	s_mov_b32 s10, 0x3e200000
	s_cselect_b32 s10, s10, 0x45200000
	s_cselect_b32 s43, s41, 0
	s_cselect_b32 s42, s11, s42
	s_add_u32 s41, s18, s10
	s_addc_u32 s44, s19, 0
	s_lshl_b64 s[10:11], s[42:43], 10
	s_add_u32 s10, s41, s10
	s_addc_u32 s11, s44, s11
	s_waitcnt vmcnt(2)
	v_lshlrev_b32_e32 v62, 16, v8
	s_waitcnt vmcnt(1)
	v_lshlrev_b32_e32 v70, 16, v12
	v_and_b32_e32 v72, 0xffff0000, v12
	v_add_f32_e32 v2, 0, v70
	v_lshlrev_b32_e32 v71, 16, v13
	v_add_f32_e32 v2, v2, v72
	v_and_b32_e32 v73, 0xffff0000, v13
	v_add_f32_e32 v2, v2, v71
	v_lshlrev_b32_e32 v74, 16, v14
	v_add_f32_e32 v2, v2, v73
	v_and_b32_e32 v76, 0xffff0000, v14
	v_add_f32_e32 v2, v2, v74
	v_lshlrev_b32_e32 v75, 16, v15
	v_add_f32_e32 v2, v2, v76
	v_and_b32_e32 v77, 0xffff0000, v15
	v_add_f32_e32 v2, v2, v75
	v_add_f32_e32 v2, v2, v77
	v_and_b32_e32 v64, 0xffff0000, v8
	v_add_f32_e32 v2, v2, v62
	v_lshlrev_b32_e32 v63, 16, v9
	v_add_f32_e32 v2, v2, v64
	v_and_b32_e32 v65, 0xffff0000, v9
	v_add_f32_e32 v2, v2, v63
	v_lshlrev_b32_e32 v66, 16, v10
	v_add_f32_e32 v2, v2, v65
	v_and_b32_e32 v68, 0xffff0000, v10
	v_add_f32_e32 v2, v2, v66
	v_lshlrev_b32_e32 v67, 16, v11
	v_add_f32_e32 v2, v2, v68
	v_and_b32_e32 v69, 0xffff0000, v11
	v_add_f32_e32 v2, v2, v67
	v_add_f32_e32 v2, v2, v69
	ds_bpermute_b32 v12, v80, v2
	global_load_dwordx4 v[8:11], v[44:45], off offset:2048
	s_waitcnt lgkmcnt(0)
	v_add_f32_e32 v2, v2, v12
	global_load_dwordx4 v[12:15], v[42:43], off offset:2064
	global_load_dwordx4 v[16:19], v[44:45], off offset:2064
	ds_bpermute_b32 v20, v81, v2
	s_waitcnt lgkmcnt(0)
	v_add_f32_e32 v2, v2, v20
	global_load_dwordx4 v[20:23], v[42:43], off offset:16
	global_load_dwordx4 v[24:27], v[42:43], off
	global_load_dwordx4 v[28:31], v[44:45], off offset:16
	global_load_dwordx4 v[32:35], v[44:45], off
	ds_bpermute_b32 v53, v82, v2
	s_waitcnt lgkmcnt(0)
	v_add_f32_e32 v2, v2, v53
	ds_bpermute_b32 v53, v83, v2
	s_waitcnt lgkmcnt(0)
	v_add_f32_e32 v2, v2, v53
	ds_bpermute_b32 v53, v84, v2
	s_waitcnt lgkmcnt(0)
	v_add_f32_e32 v2, v2, v53
	ds_bpermute_b32 v53, v85, v2
	s_waitcnt lgkmcnt(0)
	v_add_f32_e32 v2, v2, v53
	v_mul_f32_e32 v2, 0x3a800000, v2
	v_pk_add_f32 v[70:71], v[70:71], v[2:3] op_sel_hi:[1,0] neg_lo:[0,1] neg_hi:[0,1]
	v_pk_add_f32 v[72:73], v[72:73], v[2:3] op_sel_hi:[1,0] neg_lo:[0,1] neg_hi:[0,1]
	v_pk_mul_f32 v[108:109], v[70:71], v[70:71]
	v_pk_mul_f32 v[110:111], v[72:73], v[72:73]
	v_pk_add_f32 v[74:75], v[74:75], v[2:3] op_sel_hi:[1,0] neg_lo:[0,1] neg_hi:[0,1]
	v_pk_add_f32 v[76:77], v[76:77], v[2:3] op_sel_hi:[1,0] neg_lo:[0,1] neg_hi:[0,1]
	v_pk_add_f32 v[62:63], v[62:63], v[2:3] op_sel_hi:[1,0] neg_lo:[0,1] neg_hi:[0,1]
	v_pk_add_f32 v[64:65], v[64:65], v[2:3] op_sel_hi:[1,0] neg_lo:[0,1] neg_hi:[0,1]
	v_pk_add_f32 v[66:67], v[66:67], v[2:3] op_sel_hi:[1,0] neg_lo:[0,1] neg_hi:[0,1]
	v_pk_add_f32 v[68:69], v[68:69], v[2:3] op_sel_hi:[1,0] neg_lo:[0,1] neg_hi:[0,1]
	v_add_f32_e32 v2, v108, v110
	v_add_f32_e32 v2, v109, v2
	v_pk_mul_f32 v[112:113], v[74:75], v[74:75]
	v_add_f32_e32 v2, v111, v2
	v_pk_mul_f32 v[114:115], v[76:77], v[76:77]
	v_add_f32_e32 v2, v112, v2
	v_add_f32_e32 v2, v114, v2
	v_add_f32_e32 v2, v113, v2
	v_pk_mul_f32 v[116:117], v[62:63], v[62:63]
	v_add_f32_e32 v2, v115, v2
	v_pk_mul_f32 v[118:119], v[64:65], v[64:65]
	v_add_f32_e32 v2, v116, v2
	v_add_f32_e32 v2, v118, v2
	v_mov_b32_e32 v120, v68
	v_mov_b32_e32 v121, v66
	v_add_f32_e32 v2, v117, v2
	v_pk_mul_f32 v[120:121], v[120:121], v[120:121]
	v_add_f32_e32 v2, v119, v2
	v_mov_b32_e32 v122, v69
	v_mov_b32_e32 v123, v67
	v_add_f32_e32 v2, v121, v2
	v_pk_mul_f32 v[122:123], v[122:123], v[122:123]
	v_add_f32_e32 v2, v120, v2
	v_add_f32_e32 v2, v123, v2
	v_add_f32_e32 v2, v122, v2
	ds_bpermute_b32 v53, v80, v2
	s_waitcnt vmcnt(7)
	v_mov_b32_e32 v108, v4
	v_mov_b32_e32 v109, v6
	v_mov_b32_e32 v6, v5
	s_waitcnt lgkmcnt(0)
	v_add_f32_e32 v2, v2, v53
	ds_bpermute_b32 v4, v81, v2
	s_waitcnt vmcnt(6)
	v_mov_b32_e32 v110, v8
	v_mov_b32_e32 v111, v10
	v_mov_b32_e32 v10, v9
	s_waitcnt lgkmcnt(0)
	v_add_f32_e32 v2, v2, v4
	ds_bpermute_b32 v53, v82, v2
	s_waitcnt vmcnt(4)
	v_mov_b32_e32 v8, v16
	v_mov_b32_e32 v4, v12
	v_mov_b32_e32 v5, v14
	v_mov_b32_e32 v9, v18
	s_waitcnt lgkmcnt(0)
	v_add_f32_e32 v2, v2, v53
	ds_bpermute_b32 v16, v83, v2
	s_waitcnt vmcnt(2)
	v_mov_b32_e32 v12, v24
	v_mov_b32_e32 v14, v13
	v_mov_b32_e32 v18, v17
	v_mov_b32_e32 v13, v26
	s_waitcnt lgkmcnt(0)
	v_add_f32_e32 v2, v2, v16
	ds_bpermute_b32 v24, v84, v2
	s_waitcnt vmcnt(0)
	v_mov_b32_e32 v16, v32
	v_mov_b32_e32 v17, v34
	v_mov_b32_e32 v26, v25
	v_mov_b32_e32 v34, v33
	s_waitcnt lgkmcnt(0)
	v_add_f32_e32 v2, v2, v24
	ds_bpermute_b32 v53, v85, v2
	v_mov_b32_e32 v24, v20
	v_mov_b32_e32 v25, v22
	v_mov_b32_e32 v32, v28
	v_mov_b32_e32 v33, v30
	s_waitcnt lgkmcnt(0)
	v_add_f32_e32 v2, v2, v53
	v_fmamk_f32 v2, v2, 0x3a800000, v237
	v_mul_f32_e32 v20, 0x4b800000, v2
	v_cmp_gt_f32_e32 vcc, s85, v2
	v_mov_b32_e32 v22, v21
	v_mov_b32_e32 v30, v29
	v_cndmask_b32_e32 v2, v2, v20, vcc
	v_rsq_f32_e32 v2, v2
	s_nop 0
	v_mul_f32_e32 v20, 0x45800000, v2
	v_cndmask_b32_e32 v2, v2, v20, vcc
	v_pk_mul_f32 v[20:21], v[70:71], v[2:3] op_sel_hi:[1,0]
	v_pk_mul_f32 v[28:29], v[74:75], v[2:3] op_sel_hi:[1,0]
	v_pk_mul_f32 v[70:71], v[72:73], v[2:3] op_sel_hi:[1,0]
	v_pk_mul_f32 v[64:65], v[64:65], v[2:3] op_sel_hi:[1,0]
	v_pk_fma_f32 v[12:13], v[12:13], v[20:21], v[16:17]
	v_pk_fma_f32 v[16:17], v[24:25], v[28:29], v[32:33]
	v_pk_fma_f32 v[20:21], v[26:27], v[70:71], v[34:35]
	v_pk_mul_f32 v[72:73], v[76:77], v[2:3] op_sel_hi:[1,0]
	v_pk_fma_f32 v[28:29], v[6:7], v[64:65], v[10:11]
	v_bfe_u32 v6, v20, 16, 1
	v_bfe_u32 v10, v17, 16, 1
	v_max3_f32 v35, |v12|, 0, |v20|
	v_pk_fma_f32 v[22:23], v[22:23], v[72:73], v[30:31]
	v_add3_u32 v53, v20, v6, s86
	v_add3_u32 v6, v17, v10, s86
	v_max3_f32 v10, v35, |v13|, |v21|
	v_pk_mul_f32 v[62:63], v[62:63], v[2:3] op_sel_hi:[1,0]
	v_max3_f32 v10, v10, |v16|, |v22|
	v_pk_fma_f32 v[24:25], v[108:109], v[62:63], v[110:111]
	v_max3_f32 v10, v10, |v17|, |v23|
	v_pk_mul_f32 v[66:67], v[66:67], v[2:3] op_sel_hi:[1,0]
	v_pk_mul_f32 v[68:69], v[68:69], v[2:3] op_sel_hi:[1,0]
	v_max3_f32 v10, v10, |v24|, |v28|
	v_pk_fma_f32 v[26:27], v[4:5], v[66:67], v[8:9]
	v_pk_fma_f32 v[14:15], v[14:15], v[68:69], v[18:19]
	v_max3_f32 v10, v10, |v25|, |v29|
	v_max3_f32 v10, v10, |v26|, |v14|
	v_max3_f32 v10, v10, |v27|, |v15|
	ds_bpermute_b32 v35, v80, v10
	v_bfe_u32 v7, v12, 16, 1
	v_add3_u32 v7, v12, v7, s86
	v_lshrrev_b32_e32 v62, 16, v7
	v_bfe_u32 v2, v23, 16, 1
	s_waitcnt lgkmcnt(0)
	v_max_f32_e32 v35, v35, v35
	v_max_f32_e32 v10, v10, v35
	ds_bpermute_b32 v35, v81, v10
	v_add3_u32 v2, v23, v2, s86
	v_lshrrev_b32_e32 v6, 16, v6
	s_waitcnt lgkmcnt(0)
	v_max_f32_e32 v7, v35, v35
	v_max_f32_e32 v7, v10, v7
	ds_bpermute_b32 v10, v82, v7
	s_waitcnt lgkmcnt(0)
	v_max_f32_e32 v10, v10, v10
	v_max_f32_e32 v10, v7, v10
	ds_bpermute_b32 v35, v83, v10
	v_and_or_b32 v7, v2, s87, v6
	v_cvt_pk_bf16_f32 v5, v13, v21
	s_waitcnt lgkmcnt(0)
	v_max_f32_e32 v2, v35, v35
	v_max_f32_e32 v2, v10, v2
	ds_bpermute_b32 v10, v84, v2
	v_cvt_pk_bf16_f32 v11, v27, v15
	s_waitcnt lgkmcnt(0)
	v_max_f32_e32 v8, v10, v10
	v_max_f32_e32 v2, v2, v8
	ds_bpermute_b32 v34, v85, v2
	v_cvt_pk_bf16_f32 v6, v16, v22
	v_and_or_b32 v4, v53, s87, v62
	s_waitcnt lgkmcnt(0)
	v_max3_f32 v2, v2, v34, s55
	global_store_dwordx4 v[78:79], v[4:7], off
	s_nop 1
	v_div_scale_f32 v4, s[42:43], v2, v2, s80
	s_nop 0
	v_rcp_f32_e32 v5, v4
	s_nop 0
	v_fma_f32 v7, -v4, v5, 1.0
	v_div_scale_f32 v6, vcc, s80, v2, s80
	v_fmac_f32_e32 v5, v7, v5
	v_cvt_pk_bf16_f32 v10, v26, v14
	v_cvt_pk_bf16_f32 v9, v25, v29
	v_cvt_pk_bf16_f32 v8, v24, v28
	v_mul_f32_e32 v7, v6, v5
	global_store_dwordx4 v[78:79], v[8:11], off offset:1024
	s_nop 1
	v_fma_f32 v8, -v4, v7, v6
	v_fmac_f32_e32 v7, v8, v5
	v_fma_f32 v4, -v4, v7, v6
	v_div_fmas_f32 v4, v4, v5, v7
	v_div_fixup_f32 v4, v4, v2, s80
	v_mul_f32_e32 v5, v12, v4
	v_mul_f32_e32 v6, v20, v4
	v_rndne_f32_e32 v5, v5
	v_mul_f32_e32 v7, v13, v4
	v_mul_f32_e32 v8, v21, v4
	v_mul_f32_e32 v9, v16, v4
	v_mul_f32_e32 v10, v22, v4
	v_mul_f32_e32 v11, v17, v4
	v_mul_f32_e32 v12, v23, v4
	v_mul_f32_e32 v13, v24, v4
	v_mul_f32_e32 v16, v28, v4
	v_mul_f32_e32 v17, v25, v4
	v_mul_f32_e32 v18, v29, v4
	v_mul_f32_e32 v19, v26, v4
	v_mul_f32_e32 v14, v14, v4
	v_mul_f32_e32 v20, v27, v4
	v_mul_f32_e32 v4, v15, v4
	v_rndne_f32_e32 v6, v6
	v_rndne_f32_e32 v15, v4
	v_add_f32_e32 v4, 0x43000000, v5
	v_rndne_f32_e32 v7, v7
	v_cvt_pk_u8_f32 v4, v4, 0, 0
	v_add_f32_e32 v5, 0x43000000, v6
	v_rndne_f32_e32 v8, v8
	v_cvt_pk_u8_f32 v4, v5, 1, v4
	v_add_f32_e32 v5, 0x43000000, v7
	v_rndne_f32_e32 v9, v9
	v_cvt_pk_u8_f32 v4, v5, 2, v4
	v_add_f32_e32 v5, 0x43000000, v8
	v_rndne_f32_e32 v10, v10
	v_cvt_pk_u8_f32 v4, v5, 3, v4
	v_add_f32_e32 v5, 0x43000000, v9
	v_rndne_f32_e32 v11, v11
	v_cvt_pk_u8_f32 v5, v5, 0, 0
	v_add_f32_e32 v6, 0x43000000, v10
	v_rndne_f32_e32 v12, v12
	v_cvt_pk_u8_f32 v5, v6, 1, v5
	v_add_f32_e32 v6, 0x43000000, v11
	v_rndne_f32_e32 v13, v13
	v_cvt_pk_u8_f32 v5, v6, 2, v5
	v_add_f32_e32 v6, 0x43000000, v12
	v_rndne_f32_e32 v16, v16
	v_cvt_pk_u8_f32 v5, v6, 3, v5
	v_add_f32_e32 v6, 0x43000000, v13
	v_rndne_f32_e32 v17, v17
	v_cvt_pk_u8_f32 v6, v6, 0, 0
	v_add_f32_e32 v7, 0x43000000, v16
	v_rndne_f32_e32 v18, v18
	v_cvt_pk_u8_f32 v6, v7, 1, v6
	v_add_f32_e32 v7, 0x43000000, v17
	v_rndne_f32_e32 v19, v19
	v_cvt_pk_u8_f32 v6, v7, 2, v6
	v_add_f32_e32 v7, 0x43000000, v18
	v_rndne_f32_e32 v14, v14
	v_cvt_pk_u8_f32 v6, v7, 3, v6
	v_add_f32_e32 v7, 0x43000000, v19
	v_rndne_f32_e32 v20, v20
	v_cvt_pk_u8_f32 v7, v7, 0, 0
	v_add_f32_e32 v8, 0x43000000, v14
	v_cvt_pk_u8_f32 v7, v8, 1, v7
	v_add_f32_e32 v8, 0x43000000, v20
	v_cvt_pk_u8_f32 v7, v8, 2, v7
	v_add_f32_e32 v8, 0x43000000, v15
	v_xor_b32_e32 v4, 0x80808080, v4
	v_xor_b32_e32 v5, 0x80808080, v5
	v_cvt_pk_u8_f32 v7, v8, 3, v7
	v_lshl_add_u64 v[8:9], s[10:11], 0, v[38:39]
	v_xor_b32_e32 v6, 0x80808080, v6
	v_xor_b32_e32 v7, 0x80808080, v7
	global_store_dwordx2 v[8:9], v[4:5], off
	global_store_dwordx2 v[8:9], v[6:7], off offset:512
	s_and_saveexec_b64 s[10:11], s[4:5]
	s_cbranch_execz .LBB0_1206
	s_add_u32 s42, s18, s16
	s_addc_u32 s43, s19, s17
	v_mul_f32_e32 v2, 0x3c010204, v2
	global_store_dword v3, v2, s[42:43]
.LBB0_1206:
	s_or_b64 exec, exec, s[10:11]
	v_lshl_add_u64 v[78:79], s[18:19], 0, v[56:57]
	v_add_co_u32_e32 v4, vcc, 0x2f200000, v78
	s_mov_b32 s41, 0x2e00000
	s_nop 0
	v_addc_co_u32_e32 v5, vcc, 0, v79, vcc
	global_load_dwordx4 v[8:11], v[4:5], off offset:1024
	global_load_dwordx4 v[12:15], v[4:5], off
	s_nop 0
	global_load_dwordx4 v[4:7], v[42:43], off offset:2048
	v_add_co_u32_e32 v78, vcc, s41, v78
	s_add_i32 s10, s40, 2
	s_nop 0
	v_addc_co_u32_e32 v79, vcc, 0, v79, vcc
	s_add_u32 s11, s30, s8
	s_addc_u32 s41, s31, s9
	s_add_i32 s42, s40, 0xffffc002
	s_cmpk_lt_i32 s10, 0x4000
	s_mov_b32 s10, 0x3e200000
	s_cselect_b32 s10, s10, 0x45200000
	s_cselect_b32 s43, s41, 0
	s_cselect_b32 s42, s11, s42
	s_add_u32 s41, s18, s10
	s_addc_u32 s44, s19, 0
	s_lshl_b64 s[10:11], s[42:43], 10
	s_add_u32 s10, s41, s10
	s_addc_u32 s11, s44, s11
	s_waitcnt vmcnt(2)
	v_lshlrev_b32_e32 v62, 16, v8
	s_waitcnt vmcnt(1)
	v_lshlrev_b32_e32 v70, 16, v12
	v_and_b32_e32 v72, 0xffff0000, v12
	v_add_f32_e32 v2, 0, v70
	v_lshlrev_b32_e32 v71, 16, v13
	v_add_f32_e32 v2, v2, v72
	v_and_b32_e32 v73, 0xffff0000, v13
	v_add_f32_e32 v2, v2, v71
	v_lshlrev_b32_e32 v74, 16, v14
	v_add_f32_e32 v2, v2, v73
	v_and_b32_e32 v76, 0xffff0000, v14
	v_add_f32_e32 v2, v2, v74
	v_lshlrev_b32_e32 v75, 16, v15
	v_add_f32_e32 v2, v2, v76
	v_and_b32_e32 v77, 0xffff0000, v15
	v_add_f32_e32 v2, v2, v75
	v_add_f32_e32 v2, v2, v77
	v_and_b32_e32 v64, 0xffff0000, v8
	v_add_f32_e32 v2, v2, v62
	v_lshlrev_b32_e32 v63, 16, v9
	v_add_f32_e32 v2, v2, v64
	v_and_b32_e32 v65, 0xffff0000, v9
	v_add_f32_e32 v2, v2, v63
	v_lshlrev_b32_e32 v66, 16, v10
	v_add_f32_e32 v2, v2, v65
	v_and_b32_e32 v68, 0xffff0000, v10
	v_add_f32_e32 v2, v2, v66
	v_lshlrev_b32_e32 v67, 16, v11
	v_add_f32_e32 v2, v2, v68
	v_and_b32_e32 v69, 0xffff0000, v11
	v_add_f32_e32 v2, v2, v67
	v_add_f32_e32 v2, v2, v69
	ds_bpermute_b32 v12, v80, v2
	global_load_dwordx4 v[8:11], v[44:45], off offset:2048
	s_waitcnt lgkmcnt(0)
	v_add_f32_e32 v2, v2, v12
	global_load_dwordx4 v[12:15], v[42:43], off offset:2064
	global_load_dwordx4 v[16:19], v[44:45], off offset:2064
	ds_bpermute_b32 v20, v81, v2
	s_waitcnt lgkmcnt(0)
	v_add_f32_e32 v2, v2, v20
	global_load_dwordx4 v[20:23], v[42:43], off offset:16
	global_load_dwordx4 v[24:27], v[42:43], off
	global_load_dwordx4 v[28:31], v[44:45], off offset:16
	global_load_dwordx4 v[32:35], v[44:45], off
	ds_bpermute_b32 v53, v82, v2
	s_waitcnt lgkmcnt(0)
	v_add_f32_e32 v2, v2, v53
	ds_bpermute_b32 v53, v83, v2
	s_waitcnt lgkmcnt(0)
	v_add_f32_e32 v2, v2, v53
	ds_bpermute_b32 v53, v84, v2
	s_waitcnt lgkmcnt(0)
	v_add_f32_e32 v2, v2, v53
	ds_bpermute_b32 v53, v85, v2
	s_waitcnt lgkmcnt(0)
	v_add_f32_e32 v2, v2, v53
	v_mul_f32_e32 v2, 0x3a800000, v2
	v_pk_add_f32 v[70:71], v[70:71], v[2:3] op_sel_hi:[1,0] neg_lo:[0,1] neg_hi:[0,1]
	v_pk_add_f32 v[72:73], v[72:73], v[2:3] op_sel_hi:[1,0] neg_lo:[0,1] neg_hi:[0,1]
	v_pk_mul_f32 v[108:109], v[70:71], v[70:71]
	v_pk_mul_f32 v[110:111], v[72:73], v[72:73]
	v_pk_add_f32 v[74:75], v[74:75], v[2:3] op_sel_hi:[1,0] neg_lo:[0,1] neg_hi:[0,1]
	v_pk_add_f32 v[76:77], v[76:77], v[2:3] op_sel_hi:[1,0] neg_lo:[0,1] neg_hi:[0,1]
	v_pk_add_f32 v[62:63], v[62:63], v[2:3] op_sel_hi:[1,0] neg_lo:[0,1] neg_hi:[0,1]
	v_pk_add_f32 v[64:65], v[64:65], v[2:3] op_sel_hi:[1,0] neg_lo:[0,1] neg_hi:[0,1]
	v_pk_add_f32 v[66:67], v[66:67], v[2:3] op_sel_hi:[1,0] neg_lo:[0,1] neg_hi:[0,1]
	v_pk_add_f32 v[68:69], v[68:69], v[2:3] op_sel_hi:[1,0] neg_lo:[0,1] neg_hi:[0,1]
	v_add_f32_e32 v2, v108, v110
	v_add_f32_e32 v2, v109, v2
	v_pk_mul_f32 v[112:113], v[74:75], v[74:75]
	v_add_f32_e32 v2, v111, v2
	v_pk_mul_f32 v[114:115], v[76:77], v[76:77]
	v_add_f32_e32 v2, v112, v2
	v_add_f32_e32 v2, v114, v2
	v_add_f32_e32 v2, v113, v2
	v_pk_mul_f32 v[116:117], v[62:63], v[62:63]
	v_add_f32_e32 v2, v115, v2
	v_pk_mul_f32 v[118:119], v[64:65], v[64:65]
	v_add_f32_e32 v2, v116, v2
	v_add_f32_e32 v2, v118, v2
	v_mov_b32_e32 v120, v68
	v_mov_b32_e32 v121, v66
	v_add_f32_e32 v2, v117, v2
	v_pk_mul_f32 v[120:121], v[120:121], v[120:121]
	v_add_f32_e32 v2, v119, v2
	v_mov_b32_e32 v122, v69
	v_mov_b32_e32 v123, v67
	v_add_f32_e32 v2, v121, v2
	v_pk_mul_f32 v[122:123], v[122:123], v[122:123]
	v_add_f32_e32 v2, v120, v2
	v_add_f32_e32 v2, v123, v2
	v_add_f32_e32 v2, v122, v2
	ds_bpermute_b32 v53, v80, v2
	s_waitcnt vmcnt(7)
	v_mov_b32_e32 v108, v4
	v_mov_b32_e32 v109, v6
	v_mov_b32_e32 v6, v5
	s_waitcnt lgkmcnt(0)
	v_add_f32_e32 v2, v2, v53
	ds_bpermute_b32 v4, v81, v2
	s_waitcnt vmcnt(6)
	v_mov_b32_e32 v110, v8
	v_mov_b32_e32 v111, v10
	v_mov_b32_e32 v10, v9
	s_waitcnt lgkmcnt(0)
	v_add_f32_e32 v2, v2, v4
	ds_bpermute_b32 v53, v82, v2
	s_waitcnt vmcnt(4)
	v_mov_b32_e32 v8, v16
	v_mov_b32_e32 v4, v12
	v_mov_b32_e32 v5, v14
	v_mov_b32_e32 v9, v18
	s_waitcnt lgkmcnt(0)
	v_add_f32_e32 v2, v2, v53
	ds_bpermute_b32 v16, v83, v2
	s_waitcnt vmcnt(2)
	v_mov_b32_e32 v12, v24
	v_mov_b32_e32 v14, v13
	v_mov_b32_e32 v18, v17
	v_mov_b32_e32 v13, v26
	s_waitcnt lgkmcnt(0)
	v_add_f32_e32 v2, v2, v16
	ds_bpermute_b32 v24, v84, v2
	s_waitcnt vmcnt(0)
	v_mov_b32_e32 v16, v32
	v_mov_b32_e32 v17, v34
	v_mov_b32_e32 v26, v25
	v_mov_b32_e32 v34, v33
	s_waitcnt lgkmcnt(0)
	v_add_f32_e32 v2, v2, v24
	ds_bpermute_b32 v53, v85, v2
	v_mov_b32_e32 v24, v20
	v_mov_b32_e32 v25, v22
	v_mov_b32_e32 v32, v28
	v_mov_b32_e32 v33, v30
	s_waitcnt lgkmcnt(0)
	v_add_f32_e32 v2, v2, v53
	v_fmamk_f32 v2, v2, 0x3a800000, v237
	v_mul_f32_e32 v20, 0x4b800000, v2
	v_cmp_gt_f32_e32 vcc, s85, v2
	v_mov_b32_e32 v22, v21
	v_mov_b32_e32 v30, v29
	v_cndmask_b32_e32 v2, v2, v20, vcc
	v_rsq_f32_e32 v2, v2
	s_nop 0
	v_mul_f32_e32 v20, 0x45800000, v2
	v_cndmask_b32_e32 v2, v2, v20, vcc
	v_pk_mul_f32 v[20:21], v[70:71], v[2:3] op_sel_hi:[1,0]
	v_pk_mul_f32 v[28:29], v[74:75], v[2:3] op_sel_hi:[1,0]
	v_pk_mul_f32 v[70:71], v[72:73], v[2:3] op_sel_hi:[1,0]
	v_pk_mul_f32 v[64:65], v[64:65], v[2:3] op_sel_hi:[1,0]
	v_pk_fma_f32 v[12:13], v[12:13], v[20:21], v[16:17]
	v_pk_fma_f32 v[16:17], v[24:25], v[28:29], v[32:33]
	v_pk_fma_f32 v[20:21], v[26:27], v[70:71], v[34:35]
	v_pk_mul_f32 v[72:73], v[76:77], v[2:3] op_sel_hi:[1,0]
	v_pk_fma_f32 v[28:29], v[6:7], v[64:65], v[10:11]
	v_bfe_u32 v6, v20, 16, 1
	v_bfe_u32 v10, v17, 16, 1
	v_max3_f32 v35, |v12|, 0, |v20|
	v_pk_fma_f32 v[22:23], v[22:23], v[72:73], v[30:31]
	v_add3_u32 v53, v20, v6, s86
	v_add3_u32 v6, v17, v10, s86
	v_max3_f32 v10, v35, |v13|, |v21|
	v_pk_mul_f32 v[62:63], v[62:63], v[2:3] op_sel_hi:[1,0]
	v_max3_f32 v10, v10, |v16|, |v22|
	v_pk_fma_f32 v[24:25], v[108:109], v[62:63], v[110:111]
	v_max3_f32 v10, v10, |v17|, |v23|
	v_pk_mul_f32 v[66:67], v[66:67], v[2:3] op_sel_hi:[1,0]
	v_pk_mul_f32 v[68:69], v[68:69], v[2:3] op_sel_hi:[1,0]
	v_max3_f32 v10, v10, |v24|, |v28|
	v_pk_fma_f32 v[26:27], v[4:5], v[66:67], v[8:9]
	v_pk_fma_f32 v[14:15], v[14:15], v[68:69], v[18:19]
	v_max3_f32 v10, v10, |v25|, |v29|
	v_max3_f32 v10, v10, |v26|, |v14|
	v_max3_f32 v10, v10, |v27|, |v15|
	ds_bpermute_b32 v35, v80, v10
	v_bfe_u32 v7, v12, 16, 1
	v_add3_u32 v7, v12, v7, s86
	v_lshrrev_b32_e32 v62, 16, v7
	v_bfe_u32 v2, v23, 16, 1
	s_waitcnt lgkmcnt(0)
	v_max_f32_e32 v35, v35, v35
	v_max_f32_e32 v10, v10, v35
	ds_bpermute_b32 v35, v81, v10
	v_add3_u32 v2, v23, v2, s86
	v_lshrrev_b32_e32 v6, 16, v6
	s_waitcnt lgkmcnt(0)
	v_max_f32_e32 v7, v35, v35
	v_max_f32_e32 v7, v10, v7
	ds_bpermute_b32 v10, v82, v7
	s_waitcnt lgkmcnt(0)
	v_max_f32_e32 v10, v10, v10
	v_max_f32_e32 v10, v7, v10
	ds_bpermute_b32 v35, v83, v10
	v_and_or_b32 v7, v2, s87, v6
	v_cvt_pk_bf16_f32 v5, v13, v21
	s_waitcnt lgkmcnt(0)
	v_max_f32_e32 v2, v35, v35
	v_max_f32_e32 v2, v10, v2
	ds_bpermute_b32 v10, v84, v2
	v_cvt_pk_bf16_f32 v11, v27, v15
	s_waitcnt lgkmcnt(0)
	v_max_f32_e32 v8, v10, v10
	v_max_f32_e32 v2, v2, v8
	ds_bpermute_b32 v34, v85, v2
	v_cvt_pk_bf16_f32 v6, v16, v22
	v_and_or_b32 v4, v53, s87, v62
	s_waitcnt lgkmcnt(0)
	v_max3_f32 v2, v2, v34, s55
	global_store_dwordx4 v[78:79], v[4:7], off
	s_nop 1
	v_div_scale_f32 v4, s[42:43], v2, v2, s80
	s_nop 0
	v_rcp_f32_e32 v5, v4
	s_nop 0
	v_fma_f32 v7, -v4, v5, 1.0
	v_div_scale_f32 v6, vcc, s80, v2, s80
	v_fmac_f32_e32 v5, v7, v5
	v_cvt_pk_bf16_f32 v10, v26, v14
	v_cvt_pk_bf16_f32 v9, v25, v29
	v_cvt_pk_bf16_f32 v8, v24, v28
	v_mul_f32_e32 v7, v6, v5
	global_store_dwordx4 v[78:79], v[8:11], off offset:1024
	s_nop 1
	v_fma_f32 v8, -v4, v7, v6
	v_fmac_f32_e32 v7, v8, v5
	v_fma_f32 v4, -v4, v7, v6
	v_div_fmas_f32 v4, v4, v5, v7
	v_div_fixup_f32 v4, v4, v2, s80
	v_mul_f32_e32 v5, v12, v4
	v_mul_f32_e32 v6, v20, v4
	v_rndne_f32_e32 v5, v5
	v_mul_f32_e32 v7, v13, v4
	v_mul_f32_e32 v8, v21, v4
	v_mul_f32_e32 v9, v16, v4
	v_mul_f32_e32 v10, v22, v4
	v_mul_f32_e32 v11, v17, v4
	v_mul_f32_e32 v12, v23, v4
	v_mul_f32_e32 v13, v24, v4
	v_mul_f32_e32 v16, v28, v4
	v_mul_f32_e32 v17, v25, v4
	v_mul_f32_e32 v18, v29, v4
	v_mul_f32_e32 v19, v26, v4
	v_mul_f32_e32 v14, v14, v4
	v_mul_f32_e32 v20, v27, v4
	v_mul_f32_e32 v4, v15, v4
	v_rndne_f32_e32 v6, v6
	v_rndne_f32_e32 v15, v4
	v_add_f32_e32 v4, 0x43000000, v5
	v_rndne_f32_e32 v7, v7
	v_cvt_pk_u8_f32 v4, v4, 0, 0
	v_add_f32_e32 v5, 0x43000000, v6
	v_rndne_f32_e32 v8, v8
	v_cvt_pk_u8_f32 v4, v5, 1, v4
	v_add_f32_e32 v5, 0x43000000, v7
	v_rndne_f32_e32 v9, v9
	v_cvt_pk_u8_f32 v4, v5, 2, v4
	v_add_f32_e32 v5, 0x43000000, v8
	v_rndne_f32_e32 v10, v10
	v_cvt_pk_u8_f32 v4, v5, 3, v4
	v_add_f32_e32 v5, 0x43000000, v9
	v_rndne_f32_e32 v11, v11
	v_cvt_pk_u8_f32 v5, v5, 0, 0
	v_add_f32_e32 v6, 0x43000000, v10
	v_rndne_f32_e32 v12, v12
	v_cvt_pk_u8_f32 v5, v6, 1, v5
	v_add_f32_e32 v6, 0x43000000, v11
	v_rndne_f32_e32 v13, v13
	v_cvt_pk_u8_f32 v5, v6, 2, v5
	v_add_f32_e32 v6, 0x43000000, v12
	v_rndne_f32_e32 v16, v16
	v_cvt_pk_u8_f32 v5, v6, 3, v5
	v_add_f32_e32 v6, 0x43000000, v13
	v_rndne_f32_e32 v17, v17
	v_cvt_pk_u8_f32 v6, v6, 0, 0
	v_add_f32_e32 v7, 0x43000000, v16
	v_rndne_f32_e32 v18, v18
	v_cvt_pk_u8_f32 v6, v7, 1, v6
	v_add_f32_e32 v7, 0x43000000, v17
	v_rndne_f32_e32 v19, v19
	v_cvt_pk_u8_f32 v6, v7, 2, v6
	v_add_f32_e32 v7, 0x43000000, v18
	v_rndne_f32_e32 v14, v14
	v_cvt_pk_u8_f32 v6, v7, 3, v6
	v_add_f32_e32 v7, 0x43000000, v19
	v_rndne_f32_e32 v20, v20
	v_cvt_pk_u8_f32 v7, v7, 0, 0
	v_add_f32_e32 v8, 0x43000000, v14
	v_cvt_pk_u8_f32 v7, v8, 1, v7
	v_add_f32_e32 v8, 0x43000000, v20
	v_cvt_pk_u8_f32 v7, v8, 2, v7
	v_add_f32_e32 v8, 0x43000000, v15
	v_xor_b32_e32 v4, 0x80808080, v4
	v_xor_b32_e32 v5, 0x80808080, v5
	v_cvt_pk_u8_f32 v7, v8, 3, v7
	v_lshl_add_u64 v[8:9], s[10:11], 0, v[38:39]
	v_xor_b32_e32 v6, 0x80808080, v6
	v_xor_b32_e32 v7, 0x80808080, v7
	global_store_dwordx2 v[8:9], v[4:5], off
	global_store_dwordx2 v[8:9], v[6:7], off offset:512
	s_and_saveexec_b64 s[10:11], s[4:5]
	s_cbranch_execz .LBB0_1208
	s_add_u32 s42, s18, s14
	s_addc_u32 s43, s19, s15
	v_mul_f32_e32 v2, 0x3c010204, v2
	global_store_dword v3, v2, s[42:43]
.LBB0_1208:
	s_or_b64 exec, exec, s[10:11]
	v_lshl_add_u64 v[78:79], s[18:19], 0, v[54:55]
	v_add_co_u32_e32 v4, vcc, 0x2f200000, v78
	s_mov_b32 s41, 0x2e00000
	s_nop 0
	v_addc_co_u32_e32 v5, vcc, 0, v79, vcc
	global_load_dwordx4 v[8:11], v[4:5], off offset:1024
	global_load_dwordx4 v[12:15], v[4:5], off
	s_nop 0
	global_load_dwordx4 v[4:7], v[42:43], off offset:2048
	v_add_co_u32_e32 v78, vcc, s41, v78
	s_add_i32 s10, s40, 3
	s_nop 0
	v_addc_co_u32_e32 v79, vcc, 0, v79, vcc
	s_add_u32 s11, s28, s8
	s_addc_u32 s41, s29, s9
	s_addk_i32 s40, 0xc003
	s_cmpk_lt_i32 s10, 0x4000
	s_mov_b32 s10, 0x3e200000
	s_cselect_b32 s10, s10, 0x45200000
	s_cselect_b32 s41, s41, 0
	s_cselect_b32 s40, s11, s40
	s_add_u32 s42, s18, s10
	s_addc_u32 s43, s19, 0
	s_lshl_b64 s[10:11], s[40:41], 10
	s_add_u32 s10, s42, s10
	s_addc_u32 s11, s43, s11
	s_waitcnt vmcnt(2)
	v_lshlrev_b32_e32 v62, 16, v8
	s_waitcnt vmcnt(1)
	v_lshlrev_b32_e32 v70, 16, v12
	v_and_b32_e32 v72, 0xffff0000, v12
	v_add_f32_e32 v2, 0, v70
	v_lshlrev_b32_e32 v71, 16, v13
	v_add_f32_e32 v2, v2, v72
	v_and_b32_e32 v73, 0xffff0000, v13
	v_add_f32_e32 v2, v2, v71
	v_lshlrev_b32_e32 v74, 16, v14
	v_add_f32_e32 v2, v2, v73
	v_and_b32_e32 v76, 0xffff0000, v14
	v_add_f32_e32 v2, v2, v74
	v_lshlrev_b32_e32 v75, 16, v15
	v_add_f32_e32 v2, v2, v76
	v_and_b32_e32 v77, 0xffff0000, v15
	v_add_f32_e32 v2, v2, v75
	v_add_f32_e32 v2, v2, v77
	v_and_b32_e32 v64, 0xffff0000, v8
	v_add_f32_e32 v2, v2, v62
	v_lshlrev_b32_e32 v63, 16, v9
	v_add_f32_e32 v2, v2, v64
	v_and_b32_e32 v65, 0xffff0000, v9
	v_add_f32_e32 v2, v2, v63
	v_lshlrev_b32_e32 v66, 16, v10
	v_add_f32_e32 v2, v2, v65
	v_and_b32_e32 v68, 0xffff0000, v10
	v_add_f32_e32 v2, v2, v66
	v_lshlrev_b32_e32 v67, 16, v11
	v_add_f32_e32 v2, v2, v68
	v_and_b32_e32 v69, 0xffff0000, v11
	v_add_f32_e32 v2, v2, v67
	v_add_f32_e32 v2, v2, v69
	ds_bpermute_b32 v12, v80, v2
	global_load_dwordx4 v[8:11], v[44:45], off offset:2048
	s_waitcnt lgkmcnt(0)
	v_add_f32_e32 v2, v2, v12
	global_load_dwordx4 v[12:15], v[42:43], off offset:2064
	global_load_dwordx4 v[16:19], v[44:45], off offset:2064
	ds_bpermute_b32 v20, v81, v2
	s_waitcnt lgkmcnt(0)
	v_add_f32_e32 v2, v2, v20
	global_load_dwordx4 v[20:23], v[42:43], off offset:16
	global_load_dwordx4 v[24:27], v[42:43], off
	global_load_dwordx4 v[28:31], v[44:45], off offset:16
	global_load_dwordx4 v[32:35], v[44:45], off
	ds_bpermute_b32 v53, v82, v2
	s_waitcnt lgkmcnt(0)
	v_add_f32_e32 v2, v2, v53
	ds_bpermute_b32 v53, v83, v2
	s_waitcnt lgkmcnt(0)
	v_add_f32_e32 v2, v2, v53
	ds_bpermute_b32 v53, v84, v2
	s_waitcnt lgkmcnt(0)
	v_add_f32_e32 v2, v2, v53
	ds_bpermute_b32 v53, v85, v2
	s_waitcnt lgkmcnt(0)
	v_add_f32_e32 v2, v2, v53
	v_mul_f32_e32 v2, 0x3a800000, v2
	v_pk_add_f32 v[70:71], v[70:71], v[2:3] op_sel_hi:[1,0] neg_lo:[0,1] neg_hi:[0,1]
	v_pk_add_f32 v[72:73], v[72:73], v[2:3] op_sel_hi:[1,0] neg_lo:[0,1] neg_hi:[0,1]
	v_pk_mul_f32 v[108:109], v[70:71], v[70:71]
	v_pk_mul_f32 v[110:111], v[72:73], v[72:73]
	v_pk_add_f32 v[74:75], v[74:75], v[2:3] op_sel_hi:[1,0] neg_lo:[0,1] neg_hi:[0,1]
	v_pk_add_f32 v[76:77], v[76:77], v[2:3] op_sel_hi:[1,0] neg_lo:[0,1] neg_hi:[0,1]
	v_pk_add_f32 v[62:63], v[62:63], v[2:3] op_sel_hi:[1,0] neg_lo:[0,1] neg_hi:[0,1]
	v_pk_add_f32 v[64:65], v[64:65], v[2:3] op_sel_hi:[1,0] neg_lo:[0,1] neg_hi:[0,1]
	v_pk_add_f32 v[66:67], v[66:67], v[2:3] op_sel_hi:[1,0] neg_lo:[0,1] neg_hi:[0,1]
	v_pk_add_f32 v[68:69], v[68:69], v[2:3] op_sel_hi:[1,0] neg_lo:[0,1] neg_hi:[0,1]
	v_add_f32_e32 v2, v108, v110
	v_add_f32_e32 v2, v109, v2
	v_pk_mul_f32 v[112:113], v[74:75], v[74:75]
	v_add_f32_e32 v2, v111, v2
	v_pk_mul_f32 v[114:115], v[76:77], v[76:77]
	v_add_f32_e32 v2, v112, v2
	v_add_f32_e32 v2, v114, v2
	v_add_f32_e32 v2, v113, v2
	v_pk_mul_f32 v[116:117], v[62:63], v[62:63]
	v_add_f32_e32 v2, v115, v2
	v_pk_mul_f32 v[118:119], v[64:65], v[64:65]
	v_add_f32_e32 v2, v116, v2
	v_add_f32_e32 v2, v118, v2
	v_mov_b32_e32 v120, v68
	v_mov_b32_e32 v121, v66
	v_add_f32_e32 v2, v117, v2
	v_pk_mul_f32 v[120:121], v[120:121], v[120:121]
	v_add_f32_e32 v2, v119, v2
	v_mov_b32_e32 v122, v69
	v_mov_b32_e32 v123, v67
	v_add_f32_e32 v2, v121, v2
	v_pk_mul_f32 v[122:123], v[122:123], v[122:123]
	v_add_f32_e32 v2, v120, v2
	v_add_f32_e32 v2, v123, v2
	v_add_f32_e32 v2, v122, v2
	ds_bpermute_b32 v53, v80, v2
	s_waitcnt vmcnt(7)
	v_mov_b32_e32 v108, v4
	v_mov_b32_e32 v109, v6
	v_mov_b32_e32 v6, v5
	s_waitcnt lgkmcnt(0)
	v_add_f32_e32 v2, v2, v53
	ds_bpermute_b32 v4, v81, v2
	s_waitcnt vmcnt(6)
	v_mov_b32_e32 v110, v8
	v_mov_b32_e32 v111, v10
	v_mov_b32_e32 v10, v9
	s_waitcnt lgkmcnt(0)
	v_add_f32_e32 v2, v2, v4
	ds_bpermute_b32 v53, v82, v2
	s_waitcnt vmcnt(4)
	v_mov_b32_e32 v8, v16
	v_mov_b32_e32 v4, v12
	v_mov_b32_e32 v5, v14
	v_mov_b32_e32 v9, v18
	s_waitcnt lgkmcnt(0)
	v_add_f32_e32 v2, v2, v53
	ds_bpermute_b32 v16, v83, v2
	s_waitcnt vmcnt(2)
	v_mov_b32_e32 v12, v24
	v_mov_b32_e32 v14, v13
	v_mov_b32_e32 v18, v17
	v_mov_b32_e32 v13, v26
	s_waitcnt lgkmcnt(0)
	v_add_f32_e32 v2, v2, v16
	ds_bpermute_b32 v24, v84, v2
	s_waitcnt vmcnt(0)
	v_mov_b32_e32 v16, v32
	v_mov_b32_e32 v17, v34
	v_mov_b32_e32 v26, v25
	v_mov_b32_e32 v34, v33
	s_waitcnt lgkmcnt(0)
	v_add_f32_e32 v2, v2, v24
	ds_bpermute_b32 v53, v85, v2
	v_mov_b32_e32 v24, v20
	v_mov_b32_e32 v25, v22
	v_mov_b32_e32 v32, v28
	v_mov_b32_e32 v33, v30
	s_waitcnt lgkmcnt(0)
	v_add_f32_e32 v2, v2, v53
	v_fmamk_f32 v2, v2, 0x3a800000, v237
	v_mul_f32_e32 v20, 0x4b800000, v2
	v_cmp_gt_f32_e32 vcc, s85, v2
	v_mov_b32_e32 v22, v21
	v_mov_b32_e32 v30, v29
	v_cndmask_b32_e32 v2, v2, v20, vcc
	v_rsq_f32_e32 v2, v2
	s_nop 0
	v_mul_f32_e32 v20, 0x45800000, v2
	v_cndmask_b32_e32 v2, v2, v20, vcc
	v_pk_mul_f32 v[20:21], v[70:71], v[2:3] op_sel_hi:[1,0]
	v_pk_mul_f32 v[28:29], v[74:75], v[2:3] op_sel_hi:[1,0]
	v_pk_mul_f32 v[70:71], v[72:73], v[2:3] op_sel_hi:[1,0]
	v_pk_mul_f32 v[64:65], v[64:65], v[2:3] op_sel_hi:[1,0]
	v_pk_fma_f32 v[12:13], v[12:13], v[20:21], v[16:17]
	v_pk_fma_f32 v[16:17], v[24:25], v[28:29], v[32:33]
	v_pk_fma_f32 v[20:21], v[26:27], v[70:71], v[34:35]
	v_pk_mul_f32 v[72:73], v[76:77], v[2:3] op_sel_hi:[1,0]
	v_pk_fma_f32 v[28:29], v[6:7], v[64:65], v[10:11]
	v_bfe_u32 v6, v20, 16, 1
	v_bfe_u32 v10, v17, 16, 1
	v_max3_f32 v35, |v12|, 0, |v20|
	v_pk_fma_f32 v[22:23], v[22:23], v[72:73], v[30:31]
	v_add3_u32 v53, v20, v6, s86
	v_add3_u32 v6, v17, v10, s86
	v_max3_f32 v10, v35, |v13|, |v21|
	v_pk_mul_f32 v[62:63], v[62:63], v[2:3] op_sel_hi:[1,0]
	v_max3_f32 v10, v10, |v16|, |v22|
	v_pk_fma_f32 v[24:25], v[108:109], v[62:63], v[110:111]
	v_max3_f32 v10, v10, |v17|, |v23|
	v_pk_mul_f32 v[66:67], v[66:67], v[2:3] op_sel_hi:[1,0]
	v_pk_mul_f32 v[68:69], v[68:69], v[2:3] op_sel_hi:[1,0]
	v_max3_f32 v10, v10, |v24|, |v28|
	v_pk_fma_f32 v[26:27], v[4:5], v[66:67], v[8:9]
	v_pk_fma_f32 v[14:15], v[14:15], v[68:69], v[18:19]
	v_max3_f32 v10, v10, |v25|, |v29|
	v_max3_f32 v10, v10, |v26|, |v14|
	v_max3_f32 v10, v10, |v27|, |v15|
	ds_bpermute_b32 v35, v80, v10
	v_bfe_u32 v7, v12, 16, 1
	v_add3_u32 v7, v12, v7, s86
	v_lshrrev_b32_e32 v62, 16, v7
	v_bfe_u32 v2, v23, 16, 1
	s_waitcnt lgkmcnt(0)
	v_max_f32_e32 v35, v35, v35
	v_max_f32_e32 v10, v10, v35
	ds_bpermute_b32 v35, v81, v10
	v_add3_u32 v2, v23, v2, s86
	v_lshrrev_b32_e32 v6, 16, v6
	s_waitcnt lgkmcnt(0)
	v_max_f32_e32 v7, v35, v35
	v_max_f32_e32 v7, v10, v7
	ds_bpermute_b32 v10, v82, v7
	s_waitcnt lgkmcnt(0)
	v_max_f32_e32 v10, v10, v10
	v_max_f32_e32 v10, v7, v10
	ds_bpermute_b32 v35, v83, v10
	v_and_or_b32 v7, v2, s87, v6
	v_cvt_pk_bf16_f32 v5, v13, v21
	s_waitcnt lgkmcnt(0)
	v_max_f32_e32 v2, v35, v35
	v_max_f32_e32 v2, v10, v2
	ds_bpermute_b32 v10, v84, v2
	v_cvt_pk_bf16_f32 v11, v27, v15
	s_waitcnt lgkmcnt(0)
	v_max_f32_e32 v8, v10, v10
	v_max_f32_e32 v2, v2, v8
	ds_bpermute_b32 v34, v85, v2
	v_cvt_pk_bf16_f32 v6, v16, v22
	v_and_or_b32 v4, v53, s87, v62
	s_waitcnt lgkmcnt(0)
	v_max3_f32 v2, v2, v34, s55
	global_store_dwordx4 v[78:79], v[4:7], off
	s_nop 1
	v_div_scale_f32 v4, s[40:41], v2, v2, s80
	s_nop 0
	v_rcp_f32_e32 v5, v4
	s_nop 0
	v_fma_f32 v7, -v4, v5, 1.0
	v_div_scale_f32 v6, vcc, s80, v2, s80
	v_fmac_f32_e32 v5, v7, v5
	v_cvt_pk_bf16_f32 v10, v26, v14
	v_cvt_pk_bf16_f32 v9, v25, v29
	v_cvt_pk_bf16_f32 v8, v24, v28
	v_mul_f32_e32 v7, v6, v5
	global_store_dwordx4 v[78:79], v[8:11], off offset:1024
	s_nop 1
	v_fma_f32 v8, -v4, v7, v6
	v_fmac_f32_e32 v7, v8, v5
	v_fma_f32 v4, -v4, v7, v6
	v_div_fmas_f32 v4, v4, v5, v7
	v_div_fixup_f32 v4, v4, v2, s80
	v_mul_f32_e32 v5, v12, v4
	v_mul_f32_e32 v6, v20, v4
	v_rndne_f32_e32 v5, v5
	v_mul_f32_e32 v7, v13, v4
	v_mul_f32_e32 v8, v21, v4
	v_mul_f32_e32 v9, v16, v4
	v_mul_f32_e32 v10, v22, v4
	v_mul_f32_e32 v11, v17, v4
	v_mul_f32_e32 v12, v23, v4
	v_mul_f32_e32 v13, v24, v4
	v_mul_f32_e32 v16, v28, v4
	v_mul_f32_e32 v17, v25, v4
	v_mul_f32_e32 v18, v29, v4
	v_mul_f32_e32 v19, v26, v4
	v_mul_f32_e32 v14, v14, v4
	v_mul_f32_e32 v20, v27, v4
	v_mul_f32_e32 v4, v15, v4
	v_rndne_f32_e32 v6, v6
	v_rndne_f32_e32 v15, v4
	v_add_f32_e32 v4, 0x43000000, v5
	v_rndne_f32_e32 v7, v7
	v_cvt_pk_u8_f32 v4, v4, 0, 0
	v_add_f32_e32 v5, 0x43000000, v6
	v_rndne_f32_e32 v8, v8
	v_cvt_pk_u8_f32 v4, v5, 1, v4
	v_add_f32_e32 v5, 0x43000000, v7
	v_rndne_f32_e32 v9, v9
	v_cvt_pk_u8_f32 v4, v5, 2, v4
	v_add_f32_e32 v5, 0x43000000, v8
	v_rndne_f32_e32 v10, v10
	v_cvt_pk_u8_f32 v4, v5, 3, v4
	v_add_f32_e32 v5, 0x43000000, v9
	v_rndne_f32_e32 v11, v11
	v_cvt_pk_u8_f32 v5, v5, 0, 0
	v_add_f32_e32 v6, 0x43000000, v10
	v_rndne_f32_e32 v12, v12
	v_cvt_pk_u8_f32 v5, v6, 1, v5
	v_add_f32_e32 v6, 0x43000000, v11
	v_rndne_f32_e32 v13, v13
	v_cvt_pk_u8_f32 v5, v6, 2, v5
	v_add_f32_e32 v6, 0x43000000, v12
	v_rndne_f32_e32 v16, v16
	v_cvt_pk_u8_f32 v5, v6, 3, v5
	v_add_f32_e32 v6, 0x43000000, v13
	v_rndne_f32_e32 v17, v17
	v_cvt_pk_u8_f32 v6, v6, 0, 0
	v_add_f32_e32 v7, 0x43000000, v16
	v_rndne_f32_e32 v18, v18
	v_cvt_pk_u8_f32 v6, v7, 1, v6
	v_add_f32_e32 v7, 0x43000000, v17
	v_rndne_f32_e32 v19, v19
	v_cvt_pk_u8_f32 v6, v7, 2, v6
	v_add_f32_e32 v7, 0x43000000, v18
	v_rndne_f32_e32 v14, v14
	v_cvt_pk_u8_f32 v6, v7, 3, v6
	v_add_f32_e32 v7, 0x43000000, v19
	v_rndne_f32_e32 v20, v20
	v_cvt_pk_u8_f32 v7, v7, 0, 0
	v_add_f32_e32 v8, 0x43000000, v14
	v_cvt_pk_u8_f32 v7, v8, 1, v7
	v_add_f32_e32 v8, 0x43000000, v20
	v_cvt_pk_u8_f32 v7, v8, 2, v7
	v_add_f32_e32 v8, 0x43000000, v15
	v_xor_b32_e32 v4, 0x80808080, v4
	v_xor_b32_e32 v5, 0x80808080, v5
	v_cvt_pk_u8_f32 v7, v8, 3, v7
	v_lshl_add_u64 v[8:9], s[10:11], 0, v[38:39]
	v_xor_b32_e32 v6, 0x80808080, v6
	v_xor_b32_e32 v7, 0x80808080, v7
	global_store_dwordx2 v[8:9], v[4:5], off
	global_store_dwordx2 v[8:9], v[6:7], off offset:512
	s_and_saveexec_b64 s[10:11], s[4:5]
	s_cbranch_execz .LBB0_1201
	s_add_u32 s40, s18, s12
	s_addc_u32 s41, s19, s13
	v_mul_f32_e32 v2, 0x3c010204, v2
	global_store_dword v3, v2, s[40:41]
	s_branch .LBB0_1201

.LBB0_1548:
	s_waitcnt lgkmcnt(0)
	ds_read2_b32 v[8:9], v81 offset1:8
	ds_read2_b32 v[12:13], v81 offset0:33 offset1:41
	ds_read2_b32 v[14:15], v81 offset0:66 offset1:74
	ds_read2_b32 v[16:17], v81 offset0:99 offset1:107
	ds_read2_b32 v[18:19], v81 offset0:132 offset1:140
	ds_read2_b32 v[20:21], v81 offset0:165 offset1:173
	s_waitcnt lgkmcnt(5)
	s_waitcnt lgkmcnt(4)
	v_cvt_pk_bf16_f32 v4, v8, v12
	s_waitcnt lgkmcnt(3)
	s_waitcnt lgkmcnt(2)
	ds_read2_b32 v[22:23], v81 offset0:198 offset1:206
	ds_read2_b32 v[24:25], v81 offset0:231 offset1:239
	v_cvt_pk_bf16_f32 v5, v14, v16
	s_waitcnt lgkmcnt(3)
	s_waitcnt lgkmcnt(2)
	v_cvt_pk_bf16_f32 v6, v18, v20
	s_waitcnt lgkmcnt(1)
	s_waitcnt lgkmcnt(0)
	s_lshl_b32 s92, s34, 1
	v_cvt_pk_bf16_f32 v7, v22, v24
	v_or_b32_e32 v2, s33, v80
	v_lshl_add_u64 v[10:11], v[68:69], 0, s[92:93]
	v_lshlrev_b32_e32 v2, 9, v2
	v_lshl_add_u64 v[26:27], v[10:11], 0, v[2:3]
	global_store_dwordx4 v[26:27], v[4:7], off
	s_nop 1
	v_cvt_pk_bf16_f32 v4, v9, v13
	s_nop 0
	v_cvt_pk_bf16_f32 v5, v15, v17
	v_cvt_pk_bf16_f32 v6, v19, v21
	v_cvt_pk_bf16_f32 v7, v23, v25
	v_or_b32_e32 v2, s33, v82
	v_lshlrev_b32_e32 v2, 9, v2
	ds_read2_b32 v[8:9], v81 offset0:16 offset1:24
	v_lshl_add_u64 v[12:13], v[10:11], 0, v[2:3]
	global_store_dwordx4 v[12:13], v[4:7], off
	ds_read2_b32 v[12:13], v81 offset0:49 offset1:57
	ds_read2_b32 v[14:15], v81 offset0:82 offset1:90
	ds_read2_b32 v[16:17], v81 offset0:115 offset1:123
	s_waitcnt lgkmcnt(3)
	s_waitcnt lgkmcnt(2)
	ds_read2_b32 v[18:19], v81 offset0:148 offset1:156
	ds_read2_b32 v[20:21], v81 offset0:181 offset1:189
	v_cvt_pk_bf16_f32 v4, v8, v12
	s_waitcnt lgkmcnt(3)
	s_waitcnt lgkmcnt(2)
	ds_read2_b32 v[22:23], v81 offset0:214 offset1:222
	ds_read2_b32 v[24:25], v81 offset0:247 offset1:255
	v_cvt_pk_bf16_f32 v5, v14, v16
	s_waitcnt lgkmcnt(3)
	s_waitcnt lgkmcnt(2)
	v_cvt_pk_bf16_f32 v6, v18, v20
	s_waitcnt lgkmcnt(1)
	s_waitcnt lgkmcnt(0)
	v_cvt_pk_bf16_f32 v7, v22, v24
	v_or_b32_e32 v2, s33, v83
	v_lshlrev_b32_e32 v2, 9, v2
	v_lshl_add_u64 v[26:27], v[10:11], 0, v[2:3]
	global_store_dwordx4 v[26:27], v[4:7], off
	s_nop 1
	v_cvt_pk_bf16_f32 v4, v9, v13
	s_nop 0
	v_cvt_pk_bf16_f32 v5, v15, v17
	v_cvt_pk_bf16_f32 v6, v19, v21
	v_cvt_pk_bf16_f32 v7, v23, v25
	v_or_b32_e32 v2, s33, v84
	v_lshlrev_b32_e32 v2, 9, v2
	v_lshl_add_u64 v[8:9], v[10:11], 0, v[2:3]
	global_store_dwordx4 v[8:9], v[4:7], off
	s_waitcnt lgkmcnt(0)
	s_mov_b64 s[0:1], 0
	s_mov_b32 s26, 0xc000
	s_movk_i32 s27, 0x5680

.LBB0_1558:
	s_and_b32 s0, s2, 0x7c0
	v_or_b32_e32 v78, s0, v70
	v_lshl_add_u64 v[76:77], v[2:3], 1, s[8:9]
	v_lshlrev_b32_e32 v2, 11, v78
	v_lshl_add_u64 v[98:99], v[76:77], 0, v[2:3]
	s_waitcnt vmcnt(15)
	v_bfe_u32 v2, v4, 16, 1
	v_add3_u32 v2, v4, v2, s86
	s_waitcnt vmcnt(14)
	v_bfe_u32 v4, v8, 16, 1
	v_lshrrev_b32_e32 v2, 16, v2
	v_add3_u32 v4, v8, v4, s86
	v_and_or_b32 v76, v4, s87, v2
	s_waitcnt vmcnt(13)
	s_waitcnt vmcnt(12)
	v_cvt_pk_bf16_f32 v77, v12, v16
	s_waitcnt vmcnt(11)
	s_waitcnt vmcnt(10)
	v_cvt_pk_bf16_f32 v78, v20, v24
	s_waitcnt vmcnt(9)
	s_waitcnt vmcnt(8)
	v_cvt_pk_bf16_f32 v79, v28, v32
	s_waitcnt vmcnt(7)
	s_waitcnt vmcnt(6)
	global_store_dwordx4 v[98:99], v[76:79], off
	s_movk_i32 s0, 0x1000
	v_add_co_u32_e32 v8, vcc, s0, v98
	v_cvt_pk_bf16_f32 v76, v36, v40
	s_waitcnt vmcnt(6)
	s_waitcnt vmcnt(5)
	v_cvt_pk_bf16_f32 v77, v44, v48
	s_waitcnt vmcnt(4)
	s_waitcnt vmcnt(3)
	v_cvt_pk_bf16_f32 v78, v52, v56
	s_waitcnt vmcnt(2)
	s_waitcnt vmcnt(1)
	v_cvt_pk_bf16_f32 v79, v64, v60
	v_bfe_u32 v2, v5, 16, 1
	v_add3_u32 v2, v5, v2, s86
	v_bfe_u32 v4, v9, 16, 1
	v_lshrrev_b32_e32 v2, 16, v2
	v_add3_u32 v4, v9, v4, s86
	global_store_dwordx4 v[98:99], v[76:79], off offset:16
	v_addc_co_u32_e32 v9, vcc, 0, v99, vcc
	s_nop 0
	s_nop 1
	v_and_or_b32 v76, v4, s87, v2
	v_cvt_pk_bf16_f32 v77, v13, v17
	v_cvt_pk_bf16_f32 v78, v21, v25
	v_cvt_pk_bf16_f32 v79, v29, v33
	global_store_dwordx4 v[98:99], v[76:79], off offset:2048
	s_nop 1
	v_cvt_pk_bf16_f32 v76, v37, v41
	s_nop 0
	v_cvt_pk_bf16_f32 v77, v45, v49
	v_cvt_pk_bf16_f32 v78, v53, v57
	v_cvt_pk_bf16_f32 v79, v65, v61
	v_bfe_u32 v2, v6, 16, 1
	v_add3_u32 v2, v6, v2, s86
	v_bfe_u32 v4, v10, 16, 1
	v_lshrrev_b32_e32 v2, 16, v2
	v_add3_u32 v4, v10, v4, s86
	global_store_dwordx4 v[98:99], v[76:79], off offset:2064
	s_nop 1
	v_and_or_b32 v76, v4, s87, v2
	s_nop 0
	v_cvt_pk_bf16_f32 v77, v14, v18
	v_cvt_pk_bf16_f32 v78, v22, v26
	v_cvt_pk_bf16_f32 v79, v30, v34
	global_store_dwordx4 v[8:9], v[76:79], off
	s_nop 1
	v_cvt_pk_bf16_f32 v76, v38, v42
	v_cvt_pk_bf16_f32 v77, v46, v50
	v_cvt_pk_bf16_f32 v78, v54, v58
	v_cvt_pk_bf16_f32 v79, v66, v62
	v_cvt_pk_bf16_f32 v4, v7, v11
	v_cvt_pk_bf16_f32 v5, v15, v19
	v_cvt_pk_bf16_f32 v6, v23, v27
	v_cvt_pk_bf16_f32 v7, v31, v35
	global_store_dwordx4 v[8:9], v[4:7], off offset:2048
	s_nop 1
	v_cvt_pk_bf16_f32 v4, v39, v43
	s_nop 0
	v_cvt_pk_bf16_f32 v5, v47, v51
	v_cvt_pk_bf16_f32 v6, v55, v59
	v_cvt_pk_bf16_f32 v7, v67, v63
	global_store_dwordx4 v[8:9], v[76:79], off offset:16
	global_store_dwordx4 v[8:9], v[4:7], off offset:2064

.LBB0_1565:
	v_or_b32_e32 v78, s2, v70
	v_lshl_add_u64 v[76:77], v[2:3], 1, s[10:11]
	v_lshlrev_b32_e32 v2, 11, v78
	v_lshl_add_u64 v[98:99], v[76:77], 0, v[2:3]
	s_waitcnt vmcnt(1)
	v_bfe_u32 v2, v64, 16, 1
	v_add3_u32 v2, v64, v2, s86
	v_bfe_u32 v64, v8, 16, 1
	v_lshrrev_b32_e32 v2, 16, v2
	v_add3_u32 v8, v8, v64, s86
	v_and_or_b32 v76, v8, s87, v2
	v_bfe_u32 v2, v4, 16, 1
	v_add3_u32 v2, v4, v2, s86
	v_bfe_u32 v4, v20, 16, 1
	v_lshrrev_b32_e32 v2, 16, v2
	v_add3_u32 v4, v20, v4, s86
	v_and_or_b32 v77, v4, s87, v2
	v_cvt_pk_bf16_f32 v78, v16, v44
	v_cvt_pk_bf16_f32 v79, v32, v52
	global_store_dwordx4 v[98:99], v[76:79], off
	s_movk_i32 s0, 0x1000
	v_add_co_u32_e32 v8, vcc, s0, v98
	v_cvt_pk_bf16_f32 v76, v12, v36
	v_cvt_pk_bf16_f32 v77, v24, v40
	v_cvt_pk_bf16_f32 v78, v28, v56
	s_waitcnt vmcnt(1)
	v_cvt_pk_bf16_f32 v79, v48, v60
	v_bfe_u32 v2, v65, 16, 1
	v_add3_u32 v2, v65, v2, s86
	v_bfe_u32 v4, v9, 16, 1
	v_lshrrev_b32_e32 v2, 16, v2
	v_add3_u32 v4, v9, v4, s86
	global_store_dwordx4 v[98:99], v[76:79], off offset:16
	v_addc_co_u32_e32 v9, vcc, 0, v99, vcc
	s_nop 0
	s_nop 1
	v_and_or_b32 v76, v4, s87, v2
	v_cvt_pk_bf16_f32 v77, v5, v21
	v_cvt_pk_bf16_f32 v78, v17, v45
	v_cvt_pk_bf16_f32 v79, v33, v53
	global_store_dwordx4 v[98:99], v[76:79], off offset:2048
	s_nop 1
	v_cvt_pk_bf16_f32 v76, v13, v37
	s_nop 0
	v_cvt_pk_bf16_f32 v77, v25, v41
	v_cvt_pk_bf16_f32 v78, v29, v57
	v_cvt_pk_bf16_f32 v79, v49, v61
	global_store_dwordx4 v[98:99], v[76:79], off offset:2064
	s_nop 1
	v_cvt_pk_bf16_f32 v76, v66, v10
	v_cvt_pk_bf16_f32 v77, v6, v22
	v_cvt_pk_bf16_f32 v78, v18, v46
	v_cvt_pk_bf16_f32 v79, v34, v54
	global_store_dwordx4 v[8:9], v[76:79], off
	s_nop 1
	v_cvt_pk_bf16_f32 v76, v14, v38
	s_nop 0
	v_cvt_pk_bf16_f32 v77, v26, v42
	v_cvt_pk_bf16_f32 v78, v30, v58
	v_cvt_pk_bf16_f32 v79, v50, v62
	v_cvt_pk_bf16_f32 v4, v67, v11
	v_cvt_pk_bf16_f32 v5, v7, v23
	v_cvt_pk_bf16_f32 v6, v19, v47
	v_cvt_pk_bf16_f32 v7, v35, v55
	global_store_dwordx4 v[8:9], v[4:7], off offset:2048
	s_nop 1
	v_cvt_pk_bf16_f32 v4, v15, v39
	s_nop 0
	v_cvt_pk_bf16_f32 v5, v27, v43
	v_cvt_pk_bf16_f32 v6, v31, v59
	v_cvt_pk_bf16_f32 v7, v51, v63
	global_store_dwordx4 v[8:9], v[76:79], off offset:16
	global_store_dwordx4 v[8:9], v[4:7], off offset:2064

.LBB0_1572:
	v_or_b32_e32 v78, s2, v70
	v_lshl_add_u64 v[76:77], v[2:3], 1, s[14:15]
	v_lshlrev_b32_e32 v2, 11, v78
	v_lshl_add_u64 v[98:99], v[76:77], 0, v[2:3]
	s_waitcnt vmcnt(1)
	v_bfe_u32 v2, v64, 16, 1
	v_add3_u32 v2, v64, v2, s86
	v_bfe_u32 v64, v8, 16, 1
	v_lshrrev_b32_e32 v2, 16, v2
	v_add3_u32 v8, v8, v64, s86
	v_and_or_b32 v76, v8, s87, v2
	v_bfe_u32 v2, v4, 16, 1
	v_add3_u32 v2, v4, v2, s86
	v_bfe_u32 v4, v20, 16, 1
	v_lshrrev_b32_e32 v2, 16, v2
	v_add3_u32 v4, v20, v4, s86
	v_and_or_b32 v77, v4, s87, v2
	v_cvt_pk_bf16_f32 v78, v16, v44
	v_cvt_pk_bf16_f32 v79, v32, v52
	global_store_dwordx4 v[98:99], v[76:79], off
	s_movk_i32 s0, 0x1000
	v_add_co_u32_e32 v8, vcc, s0, v98
	v_cvt_pk_bf16_f32 v76, v12, v36
	v_cvt_pk_bf16_f32 v77, v24, v40
	v_cvt_pk_bf16_f32 v78, v28, v56
	s_waitcnt vmcnt(1)
	v_cvt_pk_bf16_f32 v79, v48, v60
	v_bfe_u32 v2, v65, 16, 1
	v_add3_u32 v2, v65, v2, s86
	v_bfe_u32 v4, v9, 16, 1
	v_lshrrev_b32_e32 v2, 16, v2
	v_add3_u32 v4, v9, v4, s86
	global_store_dwordx4 v[98:99], v[76:79], off offset:16
	v_addc_co_u32_e32 v9, vcc, 0, v99, vcc
	s_nop 0
	s_nop 1
	v_and_or_b32 v76, v4, s87, v2
	v_cvt_pk_bf16_f32 v77, v5, v21
	v_cvt_pk_bf16_f32 v78, v17, v45
	v_cvt_pk_bf16_f32 v79, v33, v53
	global_store_dwordx4 v[98:99], v[76:79], off offset:2048
	s_nop 1
	v_cvt_pk_bf16_f32 v76, v13, v37
	s_nop 0
	v_cvt_pk_bf16_f32 v77, v25, v41
	v_cvt_pk_bf16_f32 v78, v29, v57
	v_cvt_pk_bf16_f32 v79, v49, v61
	global_store_dwordx4 v[98:99], v[76:79], off offset:2064
	s_nop 1
	v_cvt_pk_bf16_f32 v76, v66, v10
	v_cvt_pk_bf16_f32 v77, v6, v22
	v_cvt_pk_bf16_f32 v78, v18, v46
	v_cvt_pk_bf16_f32 v79, v34, v54
	global_store_dwordx4 v[8:9], v[76:79], off
	s_nop 1
	v_cvt_pk_bf16_f32 v76, v14, v38
	s_nop 0
	v_cvt_pk_bf16_f32 v77, v26, v42
	v_cvt_pk_bf16_f32 v78, v30, v58
	v_cvt_pk_bf16_f32 v79, v50, v62
	v_cvt_pk_bf16_f32 v4, v67, v11
	v_cvt_pk_bf16_f32 v5, v7, v23
	v_cvt_pk_bf16_f32 v6, v19, v47
	v_cvt_pk_bf16_f32 v7, v35, v55
	global_store_dwordx4 v[8:9], v[4:7], off offset:2048
	s_nop 1
	v_cvt_pk_bf16_f32 v4, v15, v39
	s_nop 0
	v_cvt_pk_bf16_f32 v5, v27, v43
	v_cvt_pk_bf16_f32 v6, v31, v59
	v_cvt_pk_bf16_f32 v7, v51, v63
	global_store_dwordx4 v[8:9], v[76:79], off offset:16
	global_store_dwordx4 v[8:9], v[4:7], off offset:2064

.LBB0_1581:
	v_or_b32_e32 v78, s24, v70
	v_lshlrev_b32_e32 v2, 1, v76
	v_lshl_add_u64 v[76:77], s[16:17], 0, v[2:3]
	v_lshlrev_b32_e32 v2, 8, v78
	v_lshl_add_u64 v[98:99], v[76:77], 0, v[2:3]
	s_waitcnt vmcnt(15)
	v_bfe_u32 v2, v8, 16, 1
	v_add3_u32 v2, v8, v2, s86
	s_waitcnt vmcnt(14)
	v_bfe_u32 v8, v4, 16, 1
	v_lshrrev_b32_e32 v2, 16, v2
	v_add3_u32 v4, v4, v8, s86
	v_and_or_b32 v76, v4, s87, v2
	s_waitcnt vmcnt(13)
	s_waitcnt vmcnt(12)
	v_cvt_pk_bf16_f32 v77, v16, v12
	s_waitcnt vmcnt(11)
	s_waitcnt vmcnt(10)
	v_cvt_pk_bf16_f32 v78, v24, v20
	s_waitcnt vmcnt(9)
	s_waitcnt vmcnt(8)
	v_cvt_pk_bf16_f32 v79, v36, v28
	s_waitcnt vmcnt(7)
	s_waitcnt vmcnt(6)
	global_store_dwordx4 v[98:99], v[76:79], off
	s_nop 1
	v_cvt_pk_bf16_f32 v76, v40, v32
	s_waitcnt vmcnt(6)
	s_waitcnt vmcnt(5)
	v_cvt_pk_bf16_f32 v77, v48, v44
	s_waitcnt vmcnt(4)
	s_waitcnt vmcnt(3)
	v_cvt_pk_bf16_f32 v78, v56, v52
	s_waitcnt vmcnt(2)
	s_waitcnt vmcnt(1)
	v_cvt_pk_bf16_f32 v79, v64, v60
	v_bfe_u32 v2, v9, 16, 1
	v_add3_u32 v2, v9, v2, s86
	v_bfe_u32 v4, v5, 16, 1
	v_lshrrev_b32_e32 v2, 16, v2
	v_add3_u32 v4, v5, v4, s86
	global_store_dwordx4 v[98:99], v[76:79], off offset:16
	s_nop 1
	v_and_or_b32 v76, v4, s87, v2
	s_nop 0
	v_cvt_pk_bf16_f32 v77, v17, v13
	v_cvt_pk_bf16_f32 v78, v25, v21
	v_cvt_pk_bf16_f32 v79, v37, v29
	global_store_dwordx4 v[98:99], v[76:79], off offset:256
	s_nop 1
	v_cvt_pk_bf16_f32 v76, v41, v33
	v_cvt_pk_bf16_f32 v77, v49, v45
	v_cvt_pk_bf16_f32 v78, v57, v53
	v_cvt_pk_bf16_f32 v79, v65, v61
	v_bfe_u32 v2, v10, 16, 1
	v_add3_u32 v2, v10, v2, s86
	v_bfe_u32 v4, v6, 16, 1
	v_lshrrev_b32_e32 v2, 16, v2
	v_add3_u32 v4, v6, v4, s86
	global_store_dwordx4 v[98:99], v[76:79], off offset:272
	s_nop 1
	v_and_or_b32 v76, v4, s87, v2
	s_nop 0
	v_cvt_pk_bf16_f32 v77, v18, v14
	v_cvt_pk_bf16_f32 v78, v26, v22
	v_cvt_pk_bf16_f32 v79, v38, v30
	global_store_dwordx4 v[98:99], v[76:79], off offset:512
	s_nop 1
	v_cvt_pk_bf16_f32 v76, v42, v34
	v_cvt_pk_bf16_f32 v77, v50, v46
	v_cvt_pk_bf16_f32 v78, v58, v54
	v_cvt_pk_bf16_f32 v79, v66, v62
	v_cvt_pk_bf16_f32 v4, v11, v7
	v_cvt_pk_bf16_f32 v5, v19, v15
	v_cvt_pk_bf16_f32 v6, v27, v23
	v_cvt_pk_bf16_f32 v7, v39, v31
	global_store_dwordx4 v[98:99], v[4:7], off offset:768
	s_nop 1
	v_cvt_pk_bf16_f32 v4, v43, v35
	s_nop 0
	v_cvt_pk_bf16_f32 v5, v51, v47
	v_cvt_pk_bf16_f32 v6, v59, v55
	v_cvt_pk_bf16_f32 v7, v67, v63
	global_store_dwordx4 v[98:99], v[76:79], off offset:528
	global_store_dwordx4 v[98:99], v[4:7], off offset:784

.LBB0_1583:
	s_sub_i32 s0, 0, s30
	s_mul_hi_u32 s1, s0, 0xcccccccd
	s_lshr_b32 s1, s1, 5
	s_mul_i32 s2, s1, 40
	s_sub_i32 s0, s0, s2
	s_lshl_b32 s2, s0, 6
	s_sub_i32 s0, 0, s2
	s_lshl_b32 s1, s1, 6
	v_subrev_u32_e32 v76, s1, v85
	s_ashr_i32 s1, s0, 31
	v_lshl_add_u64 v[64:65], s[0:1], 2, v[72:73]
	v_mad_i64_i32 v[4:5], s[0:1], v76, s27, v[64:65]
	v_or_b32_e32 v2, 1, v76
	global_load_dwordx4 v[4:7], v[4:5], off offset:1664
	v_mad_i64_i32 v[8:9], s[0:1], v2, s27, v[64:65]
	global_load_dwordx4 v[8:11], v[8:9], off offset:1664
	v_or_b32_e32 v2, 2, v76
	v_mad_i64_i32 v[12:13], s[0:1], v2, s27, v[64:65]
	v_or_b32_e32 v2, 3, v76
	global_load_dwordx4 v[12:15], v[12:13], off offset:1664
	v_mad_i64_i32 v[16:17], s[0:1], v2, s27, v[64:65]
	global_load_dwordx4 v[16:19], v[16:17], off offset:1664
	v_or_b32_e32 v2, 4, v76
	v_mad_i64_i32 v[20:21], s[0:1], v2, s27, v[64:65]
	v_or_b32_e32 v2, 5, v76
	global_load_dwordx4 v[20:23], v[20:21], off offset:1664
	v_mad_i64_i32 v[24:25], s[0:1], v2, s27, v[64:65]
	global_load_dwordx4 v[24:27], v[24:25], off offset:1664
	v_or_b32_e32 v2, 6, v76
	v_mad_i64_i32 v[28:29], s[0:1], v2, s27, v[64:65]
	v_or_b32_e32 v2, 7, v76
	global_load_dwordx4 v[28:31], v[28:29], off offset:1664
	v_mad_i64_i32 v[32:33], s[0:1], v2, s27, v[64:65]
	global_load_dwordx4 v[36:39], v[32:33], off offset:1664
	v_or_b32_e32 v2, 8, v76
	v_mad_i64_i32 v[32:33], s[0:1], v2, s27, v[64:65]
	v_or_b32_e32 v2, 9, v76
	global_load_dwordx4 v[32:35], v[32:33], off offset:1664
	v_mad_i64_i32 v[40:41], s[0:1], v2, s27, v[64:65]
	global_load_dwordx4 v[40:43], v[40:41], off offset:1664
	v_or_b32_e32 v2, 10, v76
	v_mad_i64_i32 v[44:45], s[0:1], v2, s27, v[64:65]
	v_or_b32_e32 v2, 11, v76
	global_load_dwordx4 v[44:47], v[44:45], off offset:1664
	v_mad_i64_i32 v[48:49], s[0:1], v2, s27, v[64:65]
	global_load_dwordx4 v[48:51], v[48:49], off offset:1664
	v_or_b32_e32 v2, 12, v76
	v_mad_i64_i32 v[52:53], s[0:1], v2, s27, v[64:65]
	v_or_b32_e32 v2, 13, v76
	global_load_dwordx4 v[52:55], v[52:53], off offset:1664
	v_mad_i64_i32 v[56:57], s[0:1], v2, s27, v[64:65]
	global_load_dwordx4 v[56:59], v[56:57], off offset:1664
	v_or_b32_e32 v2, 14, v76
	v_mad_i64_i32 v[60:61], s[0:1], v2, s27, v[64:65]
	v_or_b32_e32 v2, 15, v76
	global_load_dwordx4 v[60:63], v[60:61], off offset:1664
	v_mad_i64_i32 v[64:65], s[0:1], v2, s27, v[64:65]
	global_load_dwordx4 v[64:67], v[64:65], off offset:1664
	v_subrev_u32_e32 v78, s2, v70
	v_ashrrev_i32_e32 v77, 31, v76
	v_ashrrev_i32_e32 v79, 31, v78
	v_lshl_add_u64 v[76:77], v[76:77], 1, s[20:21]
	v_lshlrev_b64 v[98:99], 11, v[78:79]
	v_lshl_add_u64 v[102:103], v[76:77], 0, v[98:99]
	s_waitcnt vmcnt(15)
	v_bfe_u32 v2, v4, 16, 1
	v_add3_u32 v2, v4, v2, s86
	v_lshrrev_b32_e32 v2, 16, v2
	s_waitcnt vmcnt(14)
	v_bfe_u32 v4, v8, 16, 1
	v_add3_u32 v4, v8, v4, s86
	v_and_or_b32 v98, v4, s87, v2
	s_waitcnt vmcnt(13)
	s_waitcnt vmcnt(12)
	v_cvt_pk_bf16_f32 v99, v12, v16
	s_waitcnt vmcnt(11)
	s_waitcnt vmcnt(10)
	v_cvt_pk_bf16_f32 v100, v20, v24
	s_waitcnt vmcnt(9)
	s_waitcnt vmcnt(8)
	v_cvt_pk_bf16_f32 v101, v28, v36
	global_store_dwordx4 v[102:103], v[98:101], off
	s_waitcnt vmcnt(8)
	s_waitcnt vmcnt(7)
	v_cvt_pk_bf16_f32 v98, v32, v40
	s_waitcnt vmcnt(6)
	s_waitcnt vmcnt(5)
	v_cvt_pk_bf16_f32 v99, v44, v48
	s_waitcnt vmcnt(4)
	s_waitcnt vmcnt(3)
	v_cvt_pk_bf16_f32 v100, v52, v56
	s_waitcnt vmcnt(2)
	s_waitcnt vmcnt(1)
	v_cvt_pk_bf16_f32 v101, v60, v64
	global_store_dwordx4 v[102:103], v[98:101], off offset:16
	s_nop 1
	v_or_b32_e32 v98, 1, v78
	s_nop 0
	v_ashrrev_i32_e32 v99, 31, v98
	v_lshlrev_b64 v[98:99], 11, v[98:99]
	v_lshl_add_u64 v[102:103], v[76:77], 0, v[98:99]
	v_cvt_pk_bf16_f32 v98, v5, v9
	v_cvt_pk_bf16_f32 v99, v13, v17
	v_cvt_pk_bf16_f32 v100, v21, v25
	v_cvt_pk_bf16_f32 v101, v29, v37
	global_store_dwordx4 v[102:103], v[98:101], off
	s_nop 1
	v_cvt_pk_bf16_f32 v98, v33, v41
	v_cvt_pk_bf16_f32 v99, v45, v49
	v_cvt_pk_bf16_f32 v100, v53, v57
	v_cvt_pk_bf16_f32 v101, v61, v65
	v_bfe_u32 v2, v6, 16, 1
	v_add3_u32 v2, v6, v2, s86
	v_bfe_u32 v6, v10, 16, 1
	v_lshrrev_b32_e32 v2, 16, v2
	v_add3_u32 v6, v10, v6, s86
	global_store_dwordx4 v[102:103], v[98:101], off offset:16
	v_or_b32_e32 v4, 2, v78
	v_ashrrev_i32_e32 v5, 31, v4
	v_and_or_b32 v98, v6, s87, v2
	v_cvt_pk_bf16_f32 v99, v14, v18
	v_cvt_pk_bf16_f32 v100, v22, v26
	v_cvt_pk_bf16_f32 v101, v30, v38
	v_lshlrev_b64 v[4:5], 11, v[4:5]
	v_lshl_add_u64 v[4:5], v[76:77], 0, v[4:5]
	global_store_dwordx4 v[4:5], v[98:101], off
	s_nop 1
	v_cvt_pk_bf16_f32 v98, v34, v42
	v_cvt_pk_bf16_f32 v99, v46, v50
	v_cvt_pk_bf16_f32 v100, v54, v58
	v_cvt_pk_bf16_f32 v101, v62, v66
	global_store_dwordx4 v[4:5], v[98:101], off offset:16
	v_or_b32_e32 v4, 3, v78
	v_ashrrev_i32_e32 v5, 31, v4
	v_lshlrev_b64 v[4:5], 11, v[4:5]
	v_lshl_add_u64 v[8:9], v[76:77], 0, v[4:5]
	v_cvt_pk_bf16_f32 v4, v7, v11
	v_cvt_pk_bf16_f32 v5, v15, v19
	v_cvt_pk_bf16_f32 v6, v23, v27
	v_cvt_pk_bf16_f32 v7, v31, v39
	global_store_dwordx4 v[8:9], v[4:7], off
	s_nop 1
	v_cvt_pk_bf16_f32 v4, v35, v43
	s_nop 0
	v_cvt_pk_bf16_f32 v5, v47, v51
	v_cvt_pk_bf16_f32 v6, v55, v59
	v_bfe_u32 v2, v63, 16, 1
	v_add3_u32 v2, v63, v2, s86
	v_bfe_u32 v7, v67, 16, 1
	v_lshrrev_b32_e32 v2, 16, v2
	v_add3_u32 v7, v67, v7, s86
	v_and_or_b32 v7, v7, s87, v2
	global_store_dwordx4 v[8:9], v[4:7], off offset:16
	s_branch .LBB0_1514

.LBB0_1586:
	v_or_b32_e32 v78, s2, v70
	v_lshl_add_u64 v[76:77], v[2:3], 1, s[4:5]
	v_lshlrev_b32_e32 v2, 11, v78
	v_lshl_add_u64 v[98:99], v[76:77], 0, v[2:3]
	s_waitcnt vmcnt(1)
	v_bfe_u32 v2, v64, 16, 1
	v_add3_u32 v2, v64, v2, s86
	v_bfe_u32 v64, v8, 16, 1
	v_lshrrev_b32_e32 v2, 16, v2
	v_add3_u32 v8, v8, v64, s86
	v_and_or_b32 v76, v8, s87, v2
	v_bfe_u32 v2, v4, 16, 1
	v_add3_u32 v2, v4, v2, s86
	v_bfe_u32 v4, v20, 16, 1
	v_lshrrev_b32_e32 v2, 16, v2
	v_add3_u32 v4, v20, v4, s86
	v_and_or_b32 v77, v4, s87, v2
	v_cvt_pk_bf16_f32 v78, v16, v44
	v_cvt_pk_bf16_f32 v79, v32, v52
	global_store_dwordx4 v[98:99], v[76:79], off
	s_movk_i32 s0, 0x1000
	v_add_co_u32_e32 v8, vcc, s0, v98
	v_cvt_pk_bf16_f32 v76, v12, v36
	v_cvt_pk_bf16_f32 v77, v24, v40
	v_cvt_pk_bf16_f32 v78, v28, v56
	s_waitcnt vmcnt(1)
	v_cvt_pk_bf16_f32 v79, v48, v60
	v_bfe_u32 v2, v65, 16, 1
	v_add3_u32 v2, v65, v2, s86
	v_bfe_u32 v4, v9, 16, 1
	v_lshrrev_b32_e32 v2, 16, v2
	v_add3_u32 v4, v9, v4, s86
	global_store_dwordx4 v[98:99], v[76:79], off offset:16
	v_addc_co_u32_e32 v9, vcc, 0, v99, vcc
	s_nop 0
	s_nop 1
	v_and_or_b32 v76, v4, s87, v2
	v_cvt_pk_bf16_f32 v77, v5, v21
	v_cvt_pk_bf16_f32 v78, v17, v45
	v_cvt_pk_bf16_f32 v79, v33, v53
	global_store_dwordx4 v[98:99], v[76:79], off offset:2048
	s_nop 1
	v_cvt_pk_bf16_f32 v76, v13, v37
	s_nop 0
	v_cvt_pk_bf16_f32 v77, v25, v41
	v_cvt_pk_bf16_f32 v78, v29, v57
	v_cvt_pk_bf16_f32 v79, v49, v61
	global_store_dwordx4 v[98:99], v[76:79], off offset:2064
	s_nop 1
	v_cvt_pk_bf16_f32 v76, v66, v10
	v_cvt_pk_bf16_f32 v77, v6, v22
	v_cvt_pk_bf16_f32 v78, v18, v46
	v_cvt_pk_bf16_f32 v79, v34, v54
	global_store_dwordx4 v[8:9], v[76:79], off
	s_nop 1
	v_cvt_pk_bf16_f32 v76, v14, v38
	s_nop 0
	v_cvt_pk_bf16_f32 v77, v26, v42
	v_cvt_pk_bf16_f32 v78, v30, v58
	v_cvt_pk_bf16_f32 v79, v50, v62
	v_cvt_pk_bf16_f32 v4, v67, v11
	v_cvt_pk_bf16_f32 v5, v7, v23
	v_cvt_pk_bf16_f32 v6, v19, v47
	v_cvt_pk_bf16_f32 v7, v35, v55
	global_store_dwordx4 v[8:9], v[4:7], off offset:2048
	s_nop 1
	v_cvt_pk_bf16_f32 v4, v15, v39
	s_nop 0
	v_cvt_pk_bf16_f32 v5, v27, v43
	v_cvt_pk_bf16_f32 v6, v31, v59
	v_cvt_pk_bf16_f32 v7, v51, v63
	global_store_dwordx4 v[8:9], v[76:79], off offset:16
	global_store_dwordx4 v[8:9], v[4:7], off offset:2064
	s_cbranch_execz .LBB0_1554
	s_branch .LBB0_1559
